# v33 + P4 epilogue de-serialised: per 16-row block the GDF(bj0), GDF(bj1) and GNA(bj0) gate-logit loads are issued together (one round trip instead of three)
# baseline (speedup 1.0000x reference)
; #define LAS __attribute__((address_space(3)))
; __device__ __forceinline__ unsigned pk4_fp8(float a, float b, float c, float d) { int w = 0; w = __builtin_amdgcn_cvt_pk_fp8_f32(a, b, w, false); w = __builtin_amdgcn_cvt_pk_fp8_f32(c, d, w, true); return (unsigned)w; }
; __device__ __forceinline__ float bf_lo(unsigned w) { return __uint_as_float(w << 16); }
; __device__ __forceinline__ float bf_hi(unsigned w) { return __uint_as_float(w & 0xffff0000u); }
; __device__ __forceinline__ float sigmoidf_fast(float x) { return __builtin_amdgcn_rcpf(1.0f + __builtin_amdgcn_exp2f(-1.4426950408889634f * x)); }
;     __device__ __forceinline__ void operator()(f32x4 (&acc)[2][2][4][2], const Unit& u, int wr, int wc, int fr, int fq) const {
;     ...
;             for (int m = 0; m < 4; ++m) {
;                 const size_t ro = (size_t)(u.row0 + ai * 128 + wr * 64 + m * 16 + fr) * DM + col0;
; #pragma unroll
;                 for (int bj = 0; bj < 2; ++bj) {
;                     const u32x4 gd = *(const u32x4*)(GDF + ro + bj * 32);
;                     const float ed[8] = {bf_lo(gd.x), bf_hi(gd.x), bf_lo(gd.y), bf_hi(gd.y), bf_lo(gd.z), bf_hi(gd.z), bf_lo(gd.w), bf_hi(gd.w)};
;                     if (u.tag == 0) {
;                         const u32x4 gn = *(const u32x4*)(GNA + ro + bj * 32);
;                         const float en[8] = {bf_lo(gn.x), bf_hi(gn.x), bf_lo(gn.y), bf_hi(gn.y), bf_lo(gn.z), bf_hi(gn.z), bf_lo(gn.w), bf_hi(gn.w)};
; #pragma unroll
;                         for (int e = 0; e < 8; ++e) {
;                             const float r = (1.0f + __builtin_amdgcn_exp2f(-1.4426950408889634f * ed[e])) * __builtin_amdgcn_rcpf(1.0f + __builtin_amdgcn_exp2f(-1.4426950408889634f * en[e]));
;                             acc[ai][bj][m][e >> 2][e & 3] *= r; }
;                     } else {
;                         float y[8];
; #pragma unroll
;                         for (int e = 0; e < 8; ++e) y[e] = acc[ai][bj][m][e >> 2][e & 3] * sigmoidf_fast(ed[e]) * (PSCALE * WSCALE_INV * OSCALE_INV);
;                         u32x2 w; w.x = pk4_fp8(y[0], y[1], y[2], y[3]); w.y = pk4_fp8(y[4], y[5], y[6], y[7]);
;                         *(LAS u32x2*)(my + fr * 80 + bj * 32 + fq * 8) = w;
.LBB0_561:
	s_nop 15
	s_nop 15
	v_add_u32_e32 v4, s76, v164
	v_add_u32_e32 v2, s54, v167
	v_ashrrev_i32_e32 v5, 31, v4
	v_ashrrev_i32_e32 v3, 31, v2
	v_lshlrev_b64 v[6:7], 11, v[4:5]
	v_lshl_add_u64 v[8:9], v[6:7], 0, v[2:3]
	v_lshl_add_u64 v[6:7], v[8:9], 1, s[40:41]
	global_load_dwordx4 v[156:159], v[6:7], off nt
	global_load_dwordx4 v[240:243], v[6:7], off offset:64 nt
	v_lshl_add_u64 v[252:253], v[8:9], 1, s[38:39]
	global_load_dwordx4 v[244:247], v[252:253], off nt
	v_cndmask_b32_e64 v5, 0, 1, s[58:59]
	v_cmp_ne_u32_e64 s[4:5], 1, v5
	s_andn2_b64 vcc, exec, s[58:59]
	s_mov_b64 s[58:59], -1
	s_waitcnt vmcnt(0)
	v_lshlrev_b32_e32 v160, 16, v156
	v_and_b32_e32 v156, 0xffff0000, v156
	v_lshlrev_b32_e32 v161, 16, v157
	v_and_b32_e32 v157, 0xffff0000, v157
	v_lshlrev_b32_e32 v162, 16, v158
	v_and_b32_e32 v158, 0xffff0000, v158
	v_lshlrev_b32_e32 v163, 16, v159
	v_and_b32_e32 v159, 0xffff0000, v159
	v_mul_f32_e32 v160, 0xbfb8aa3b, v160
	v_mul_f32_e32 v156, 0xbfb8aa3b, v156
	v_mul_f32_e32 v181, 0xbfb8aa3b, v161
	v_mul_f32_e32 v157, 0xbfb8aa3b, v157
	v_mul_f32_e32 v182, 0xbfb8aa3b, v162
	v_mul_f32_e32 v158, 0xbfb8aa3b, v158
	v_mul_f32_e32 v183, 0xbfb8aa3b, v163
	v_mul_f32_e32 v159, 0xbfb8aa3b, v159
	v_exp_f32_e32 v160, v160
	v_exp_f32_e32 v161, v156
	v_exp_f32_e32 v162, v181
	v_exp_f32_e32 v163, v157
	v_exp_f32_e32 v156, v182
	v_exp_f32_e32 v157, v158
	v_exp_f32_e32 v158, v183
	v_exp_f32_e32 v159, v159
	s_cbranch_vccnz .LBB0_563
	v_add_f32_e32 v182, 1.0, v162
	v_rcp_f32_e32 v182, v182
	v_add_f32_e32 v183, 1.0, v163
	v_rcp_f32_e32 v183, v183
	v_add_f32_e32 v184, 1.0, v156
	v_rcp_f32_e32 v184, v184
	v_mul_f32_e32 v182, v136, v182
	v_mul_f32_e32 v185, 0x3c000000, v182
	v_mul_f32_e32 v182, v137, v183
	v_add_f32_e32 v183, 1.0, v157
	v_mul_f32_e32 v186, 0x3c000000, v182
	v_mul_f32_e32 v182, v130, v184
	v_rcp_f32_e32 v183, v183
	v_add_f32_e32 v184, 1.0, v158
	v_rcp_f32_e32 v184, v184
	v_add_f32_e32 v5, 1.0, v160
	v_add_f32_e32 v181, 1.0, v161
	v_rcp_f32_e32 v5, v5
	v_rcp_f32_e32 v181, v181
	v_mul_f32_e32 v187, 0x3c000000, v182
	v_mul_f32_e32 v182, v131, v183
	v_mul_f32_e32 v188, 0x3c000000, v182
	v_mul_f32_e32 v182, v132, v184
	v_mul_f32_e32 v184, 0x3c000000, v182
	v_add_f32_e32 v182, 1.0, v159
	v_mul_f32_e32 v5, v134, v5
	v_mul_f32_e32 v181, v135, v181
	v_rcp_f32_e32 v189, v182
	v_mul_f32_e32 v5, 0x3c000000, v5
	v_mul_f32_e32 v181, 0x3c000000, v181
	v_mov_b32_e32 v182, 0
	v_mov_b32_e32 v183, 0
	v_cvt_pk_fp8_f32 v182, v5, v181
	v_cvt_pk_fp8_f32 v183, v187, v188
	v_mul_f32_e32 v5, v133, v189
	v_mul_f32_e32 v5, 0x3c000000, v5
	v_cvt_pk_fp8_f32 v182, v185, v186 op_sel:[0,0,1]
	v_cvt_pk_fp8_f32 v183, v184, v5 op_sel:[0,0,1]
	s_mov_b64 s[58:59], 0
	ds_write_b64 v180, v[182:183]
.LBB0_563:
	s_andn2_b64 vcc, exec, s[58:59]
	v_lshl_add_u64 v[8:9], v[8:9], 1, s[38:39]
	s_cbranch_vccnz .LBB0_565
	v_mov_b64_e32 v[182:183], v[244:245]
	v_mov_b64_e32 v[184:185], v[246:247]
	v_pk_add_f32 v[162:163], v[162:163], 1.0 op_sel_hi:[1,0]
	v_pk_add_f32 v[160:161], v[160:161], 1.0 op_sel_hi:[1,0]
	v_pk_add_f32 v[158:159], v[158:159], 1.0 op_sel_hi:[1,0]
	v_pk_add_f32 v[156:157], v[156:157], 1.0 op_sel_hi:[1,0]
	s_waitcnt vmcnt(0)
	v_lshlrev_b32_e32 v5, 16, v182
	v_and_b32_e32 v181, 0xffff0000, v182
	v_lshlrev_b32_e32 v182, 16, v183
	v_and_b32_e32 v183, 0xffff0000, v183
	v_lshlrev_b32_e32 v186, 16, v184
	v_and_b32_e32 v184, 0xffff0000, v184
	v_lshlrev_b32_e32 v187, 16, v185
	v_and_b32_e32 v185, 0xffff0000, v185
	v_mul_f32_e32 v5, 0xbfb8aa3b, v5
	v_mul_f32_e32 v181, 0xbfb8aa3b, v181
	v_mul_f32_e32 v182, 0xbfb8aa3b, v182
	v_mul_f32_e32 v183, 0xbfb8aa3b, v183
	v_mul_f32_e32 v186, 0xbfb8aa3b, v186
	v_mul_f32_e32 v184, 0xbfb8aa3b, v184
	v_mul_f32_e32 v187, 0xbfb8aa3b, v187
	v_mul_f32_e32 v185, 0xbfb8aa3b, v185
	v_exp_f32_e32 v5, v5
	v_exp_f32_e32 v181, v181
	v_exp_f32_e32 v182, v182
	v_exp_f32_e32 v183, v183
	v_exp_f32_e32 v186, v186
	v_exp_f32_e32 v184, v184
	v_exp_f32_e32 v187, v187
	v_exp_f32_e32 v185, v185
	v_add_f32_e32 v5, 1.0, v5
	v_add_f32_e32 v181, 1.0, v181
	v_add_f32_e32 v188, 1.0, v182
	v_add_f32_e32 v189, 1.0, v183
	v_add_f32_e32 v186, 1.0, v186
	v_add_f32_e32 v190, 1.0, v184
	v_add_f32_e32 v191, 1.0, v187
	v_add_f32_e32 v192, 1.0, v185
	v_rcp_f32_e32 v182, v5
	v_rcp_f32_e32 v183, v181
	v_rcp_f32_e32 v184, v188
	v_rcp_f32_e32 v185, v189
	v_rcp_f32_e32 v186, v186
	v_rcp_f32_e32 v187, v190
	v_rcp_f32_e32 v188, v191
	v_rcp_f32_e32 v189, v192
	v_pk_mul_f32 v[160:161], v[160:161], v[182:183]
	v_pk_mul_f32 v[162:163], v[162:163], v[184:185]
	v_pk_mul_f32 v[156:157], v[156:157], v[186:187]
	v_pk_mul_f32 v[158:159], v[158:159], v[188:189]
	v_pk_mul_f32 v[136:137], v[136:137], v[162:163]
	v_pk_mul_f32 v[134:135], v[134:135], v[160:161]
	v_pk_mul_f32 v[132:133], v[132:133], v[158:159]
	v_pk_mul_f32 v[130:131], v[130:131], v[156:157]
.LBB0_565:
	v_mov_b64_e32 v[156:157], v[240:241]
	v_mov_b64_e32 v[158:159], v[242:243]
	s_and_b64 vcc, exec, s[4:5]
	s_mov_b64 s[58:59], -1
	s_waitcnt vmcnt(0)
	v_lshlrev_b32_e32 v5, 16, v156
	v_and_b32_e32 v6, 0xffff0000, v156
	v_lshlrev_b32_e32 v7, 16, v157
	v_and_b32_e32 v156, 0xffff0000, v157
	v_lshlrev_b32_e32 v157, 16, v158
	v_and_b32_e32 v158, 0xffff0000, v158
	v_lshlrev_b32_e32 v160, 16, v159
	v_and_b32_e32 v159, 0xffff0000, v159
	v_mul_f32_e32 v5, 0xbfb8aa3b, v5
	v_mul_f32_e32 v6, 0xbfb8aa3b, v6
	v_mul_f32_e32 v7, 0xbfb8aa3b, v7
	v_mul_f32_e32 v156, 0xbfb8aa3b, v156
	v_mul_f32_e32 v157, 0xbfb8aa3b, v157
	v_mul_f32_e32 v162, 0xbfb8aa3b, v158
	v_mul_f32_e32 v163, 0xbfb8aa3b, v160
	v_mul_f32_e32 v181, 0xbfb8aa3b, v159
	v_exp_f32_e32 v158, v5
	v_exp_f32_e32 v159, v6
	v_exp_f32_e32 v160, v7
	v_exp_f32_e32 v161, v156
	v_exp_f32_e32 v6, v157
	v_exp_f32_e32 v7, v162
	v_exp_f32_e32 v156, v163
	v_exp_f32_e32 v157, v181
	s_cbranch_vccnz .LBB0_624
	v_add_f32_e32 v162, 1.0, v159
	v_add_f32_e32 v163, 1.0, v160
	v_rcp_f32_e32 v162, v162
	v_rcp_f32_e32 v163, v163
	v_add_f32_e32 v182, 1.0, v6
	v_rcp_f32_e32 v182, v182
	v_mul_f32_e32 v162, v103, v162
	v_mul_f32_e32 v181, 0x3c000000, v162
	v_mul_f32_e32 v162, v104, v163
	v_add_f32_e32 v163, 1.0, v161
	v_rcp_f32_e32 v163, v163
	v_mul_f32_e32 v183, 0x3c000000, v162
	v_add_f32_e32 v5, 1.0, v158
	v_rcp_f32_e32 v5, v5
	v_mul_f32_e32 v162, v105, v163
	v_add_f32_e32 v163, 1.0, v7
	v_mul_f32_e32 v184, 0x3c000000, v162
	v_mul_f32_e32 v162, v98, v182
	v_rcp_f32_e32 v163, v163
	v_add_f32_e32 v182, 1.0, v156
	v_rcp_f32_e32 v182, v182
	v_mul_f32_e32 v185, 0x3c000000, v162
	v_mul_f32_e32 v162, v99, v163
	v_mul_f32_e32 v186, 0x3c000000, v162
	v_mul_f32_e32 v162, v100, v182
	v_mul_f32_e32 v182, 0x3c000000, v162
	v_add_f32_e32 v162, 1.0, v157
	v_mul_f32_e32 v5, v102, v5
	v_rcp_f32_e32 v187, v162
	v_mul_f32_e32 v5, 0x3c000000, v5
	v_mov_b32_e32 v162, 0
	v_mov_b32_e32 v163, 0
	v_cvt_pk_fp8_f32 v162, v5, v181
	v_cvt_pk_fp8_f32 v163, v185, v186
	v_mul_f32_e32 v5, v101, v187
	v_mul_f32_e32 v5, 0x3c000000, v5
	v_cvt_pk_fp8_f32 v162, v183, v184 op_sel:[0,0,1]
	v_cvt_pk_fp8_f32 v163, v182, v5 op_sel:[0,0,1]
	ds_write_b64 v180, v[162:163] offset:32
	s_cbranch_execz .LBB0_625

; #define LAS __attribute__((address_space(3)))
; __device__ __forceinline__ unsigned pk4_fp8(float a, float b, float c, float d) { int w = 0; w = __builtin_amdgcn_cvt_pk_fp8_f32(a, b, w, false); w = __builtin_amdgcn_cvt_pk_fp8_f32(c, d, w, true); return (unsigned)w; }
; __device__ __forceinline__ float bf_lo(unsigned w) { return __uint_as_float(w << 16); }
; __device__ __forceinline__ float bf_hi(unsigned w) { return __uint_as_float(w & 0xffff0000u); }
; __device__ __forceinline__ float sigmoidf_fast(float x) { return __builtin_amdgcn_rcpf(1.0f + __builtin_amdgcn_exp2f(-1.4426950408889634f * x)); }
;     __device__ __forceinline__ void operator()(f32x4 (&acc)[2][2][4][2], const Unit& u, int wr, int wc, int fr, int fq) const {
;     ...
;             for (int m = 0; m < 4; ++m) {
;                 const size_t ro = (size_t)(u.row0 + ai * 128 + wr * 64 + m * 16 + fr) * DM + col0;
; #pragma unroll
;                 for (int bj = 0; bj < 2; ++bj) {
;                     const u32x4 gd = *(const u32x4*)(GDF + ro + bj * 32);
;                     const float ed[8] = {bf_lo(gd.x), bf_hi(gd.x), bf_lo(gd.y), bf_hi(gd.y), bf_lo(gd.z), bf_hi(gd.z), bf_lo(gd.w), bf_hi(gd.w)};
;                     if (u.tag == 0) {
;                         const u32x4 gn = *(const u32x4*)(GNA + ro + bj * 32);
;                         const float en[8] = {bf_lo(gn.x), bf_hi(gn.x), bf_lo(gn.y), bf_hi(gn.y), bf_lo(gn.z), bf_hi(gn.z), bf_lo(gn.w), bf_hi(gn.w)};
; #pragma unroll
;                         for (int e = 0; e < 8; ++e) {
;                             const float r = (1.0f + __builtin_amdgcn_exp2f(-1.4426950408889634f * ed[e])) * __builtin_amdgcn_rcpf(1.0f + __builtin_amdgcn_exp2f(-1.4426950408889634f * en[e]));
;                             acc[ai][bj][m][e >> 2][e & 3] *= r; }
;                     } else {
;                         float y[8];
; #pragma unroll
;                         for (int e = 0; e < 8; ++e) y[e] = acc[ai][bj][m][e >> 2][e & 3] * sigmoidf_fast(ed[e]) * (PSCALE * WSCALE_INV * OSCALE_INV);
;                         u32x2 w; w.x = pk4_fp8(y[0], y[1], y[2], y[3]); w.y = pk4_fp8(y[4], y[5], y[6], y[7]);
;                         *(LAS u32x2*)(my + fr * 80 + bj * 32 + fq * 8) = w;
.LBB0_569:
	s_nop 1
	v_add_u32_e32 v6, s76, v168
	v_ashrrev_i32_e32 v7, 31, v6
	v_lshlrev_b64 v[6:7], 11, v[6:7]
	v_lshl_add_u64 v[6:7], v[6:7], 0, v[2:3]
	v_lshl_add_u64 v[8:9], v[6:7], 1, s[40:41]
	global_load_dwordx4 v[156:159], v[8:9], off nt
	global_load_dwordx4 v[240:243], v[8:9], off offset:64 nt
	v_lshl_add_u64 v[252:253], v[6:7], 1, s[38:39]
	global_load_dwordx4 v[244:247], v[252:253], off nt
	s_and_b64 vcc, exec, s[4:5]
	s_mov_b64 s[58:59], -1
	s_waitcnt vmcnt(0)
	v_lshlrev_b32_e32 v5, 16, v156
	v_and_b32_e32 v156, 0xffff0000, v156
	v_lshlrev_b32_e32 v160, 16, v157
	v_and_b32_e32 v157, 0xffff0000, v157
	v_lshlrev_b32_e32 v161, 16, v158
	v_and_b32_e32 v158, 0xffff0000, v158
	v_lshlrev_b32_e32 v162, 16, v159
	v_and_b32_e32 v159, 0xffff0000, v159
	v_mul_f32_e32 v5, 0xbfb8aa3b, v5
	v_mul_f32_e32 v156, 0xbfb8aa3b, v156
	v_mul_f32_e32 v163, 0xbfb8aa3b, v160
	v_mul_f32_e32 v157, 0xbfb8aa3b, v157
	v_mul_f32_e32 v181, 0xbfb8aa3b, v161
	v_mul_f32_e32 v158, 0xbfb8aa3b, v158
	v_mul_f32_e32 v182, 0xbfb8aa3b, v162
	v_mul_f32_e32 v159, 0xbfb8aa3b, v159
	v_exp_f32_e32 v160, v5
	v_exp_f32_e32 v161, v156
	v_exp_f32_e32 v162, v163
	v_exp_f32_e32 v163, v157
	v_exp_f32_e32 v156, v181
	v_exp_f32_e32 v157, v158
	v_exp_f32_e32 v158, v182
	v_exp_f32_e32 v159, v159
	s_cbranch_vccnz .LBB0_571
	v_add_f32_e32 v182, 1.0, v162
	v_rcp_f32_e32 v182, v182
	v_add_f32_e32 v183, 1.0, v163
	v_rcp_f32_e32 v183, v183
	v_add_f32_e32 v184, 1.0, v156
	v_rcp_f32_e32 v184, v184
	v_mul_f32_e32 v182, v128, v182
	v_mul_f32_e32 v185, 0x3c000000, v182
	v_mul_f32_e32 v182, v129, v183
	v_add_f32_e32 v183, 1.0, v157
	v_mul_f32_e32 v186, 0x3c000000, v182
	v_mul_f32_e32 v182, v122, v184
	v_rcp_f32_e32 v183, v183
	v_add_f32_e32 v184, 1.0, v158
	v_rcp_f32_e32 v184, v184
	v_add_f32_e32 v5, 1.0, v160
	v_add_f32_e32 v181, 1.0, v161
	v_rcp_f32_e32 v5, v5
	v_rcp_f32_e32 v181, v181
	v_mul_f32_e32 v187, 0x3c000000, v182
	v_mul_f32_e32 v182, v123, v183
	v_mul_f32_e32 v188, 0x3c000000, v182
	v_mul_f32_e32 v182, v124, v184
	v_mul_f32_e32 v184, 0x3c000000, v182
	v_add_f32_e32 v182, 1.0, v159
	v_mul_f32_e32 v5, v126, v5
	v_mul_f32_e32 v181, v127, v181
	v_rcp_f32_e32 v189, v182
	v_mul_f32_e32 v5, 0x3c000000, v5
	v_mul_f32_e32 v181, 0x3c000000, v181
	v_mov_b32_e32 v182, 0
	v_mov_b32_e32 v183, 0
	v_cvt_pk_fp8_f32 v182, v5, v181
	v_cvt_pk_fp8_f32 v183, v187, v188
	v_mul_f32_e32 v5, v125, v189
	v_mul_f32_e32 v5, 0x3c000000, v5
	v_cvt_pk_fp8_f32 v182, v185, v186 op_sel:[0,0,1]
	v_cvt_pk_fp8_f32 v183, v184, v5 op_sel:[0,0,1]
	s_mov_b64 s[58:59], 0
	ds_write_b64 v180, v[182:183]
.LBB0_571:
	s_andn2_b64 vcc, exec, s[58:59]
	v_lshl_add_u64 v[6:7], v[6:7], 1, s[38:39]
	s_cbranch_vccnz .LBB0_573
	v_mov_b64_e32 v[182:183], v[244:245]
	v_mov_b64_e32 v[184:185], v[246:247]
	v_pk_add_f32 v[162:163], v[162:163], 1.0 op_sel_hi:[1,0]
	v_pk_add_f32 v[160:161], v[160:161], 1.0 op_sel_hi:[1,0]
	v_pk_add_f32 v[158:159], v[158:159], 1.0 op_sel_hi:[1,0]
	v_pk_add_f32 v[156:157], v[156:157], 1.0 op_sel_hi:[1,0]
	s_waitcnt vmcnt(0)
	v_lshlrev_b32_e32 v5, 16, v182
	v_and_b32_e32 v181, 0xffff0000, v182
	v_lshlrev_b32_e32 v182, 16, v183
	v_and_b32_e32 v183, 0xffff0000, v183
	v_lshlrev_b32_e32 v186, 16, v184
	v_and_b32_e32 v184, 0xffff0000, v184
	v_lshlrev_b32_e32 v187, 16, v185
	v_and_b32_e32 v185, 0xffff0000, v185
	v_mul_f32_e32 v5, 0xbfb8aa3b, v5
	v_mul_f32_e32 v181, 0xbfb8aa3b, v181
	v_mul_f32_e32 v182, 0xbfb8aa3b, v182
	v_mul_f32_e32 v183, 0xbfb8aa3b, v183
	v_mul_f32_e32 v186, 0xbfb8aa3b, v186
	v_mul_f32_e32 v184, 0xbfb8aa3b, v184
	v_mul_f32_e32 v187, 0xbfb8aa3b, v187
	v_mul_f32_e32 v185, 0xbfb8aa3b, v185
	v_exp_f32_e32 v5, v5
	v_exp_f32_e32 v181, v181
	v_exp_f32_e32 v182, v182
	v_exp_f32_e32 v183, v183
	v_exp_f32_e32 v186, v186
	v_exp_f32_e32 v184, v184
	v_exp_f32_e32 v187, v187
	v_exp_f32_e32 v185, v185
	v_add_f32_e32 v5, 1.0, v5
	v_add_f32_e32 v181, 1.0, v181
	v_add_f32_e32 v188, 1.0, v182
	v_add_f32_e32 v189, 1.0, v183
	v_add_f32_e32 v186, 1.0, v186
	v_add_f32_e32 v190, 1.0, v184
	v_add_f32_e32 v191, 1.0, v187
	v_add_f32_e32 v192, 1.0, v185
	v_rcp_f32_e32 v182, v5
	v_rcp_f32_e32 v183, v181
	v_rcp_f32_e32 v184, v188
	v_rcp_f32_e32 v185, v189
	v_rcp_f32_e32 v186, v186
	v_rcp_f32_e32 v187, v190
	v_rcp_f32_e32 v188, v191
	v_rcp_f32_e32 v189, v192
	v_pk_mul_f32 v[160:161], v[160:161], v[182:183]
	v_pk_mul_f32 v[162:163], v[162:163], v[184:185]
	v_pk_mul_f32 v[156:157], v[156:157], v[186:187]
	v_pk_mul_f32 v[158:159], v[158:159], v[188:189]
	v_pk_mul_f32 v[128:129], v[128:129], v[162:163]
	v_pk_mul_f32 v[126:127], v[126:127], v[160:161]
	v_pk_mul_f32 v[124:125], v[124:125], v[158:159]
	v_pk_mul_f32 v[122:123], v[122:123], v[156:157]
.LBB0_573:
	v_mov_b64_e32 v[156:157], v[240:241]
	v_mov_b64_e32 v[158:159], v[242:243]
	s_and_b64 vcc, exec, s[4:5]
	s_mov_b64 s[58:59], -1
	s_waitcnt vmcnt(0)
	v_lshlrev_b32_e32 v5, 16, v156
	v_and_b32_e32 v8, 0xffff0000, v156
	v_lshlrev_b32_e32 v9, 16, v157
	v_and_b32_e32 v156, 0xffff0000, v157
	v_lshlrev_b32_e32 v157, 16, v158
	v_and_b32_e32 v158, 0xffff0000, v158
	v_lshlrev_b32_e32 v160, 16, v159
	v_and_b32_e32 v159, 0xffff0000, v159
	v_mul_f32_e32 v5, 0xbfb8aa3b, v5
	v_mul_f32_e32 v8, 0xbfb8aa3b, v8
	v_mul_f32_e32 v9, 0xbfb8aa3b, v9
	v_mul_f32_e32 v156, 0xbfb8aa3b, v156
	v_mul_f32_e32 v157, 0xbfb8aa3b, v157
	v_mul_f32_e32 v162, 0xbfb8aa3b, v158
	v_mul_f32_e32 v163, 0xbfb8aa3b, v160
	v_mul_f32_e32 v181, 0xbfb8aa3b, v159
	v_exp_f32_e32 v158, v5
	v_exp_f32_e32 v159, v8
	v_exp_f32_e32 v160, v9
	v_exp_f32_e32 v161, v156
	v_exp_f32_e32 v8, v157
	v_exp_f32_e32 v9, v162
	v_exp_f32_e32 v156, v163
	v_exp_f32_e32 v157, v181
	s_cbranch_vccnz .LBB0_626
	v_add_f32_e32 v162, 1.0, v159
	v_add_f32_e32 v163, 1.0, v160
	v_rcp_f32_e32 v162, v162
	v_rcp_f32_e32 v163, v163
	v_add_f32_e32 v182, 1.0, v8
	v_rcp_f32_e32 v182, v182
	v_mul_f32_e32 v162, v95, v162
	v_mul_f32_e32 v181, 0x3c000000, v162
	v_mul_f32_e32 v162, v96, v163
	v_add_f32_e32 v163, 1.0, v161
	v_rcp_f32_e32 v163, v163
	v_mul_f32_e32 v183, 0x3c000000, v162
	v_add_f32_e32 v5, 1.0, v158
	v_rcp_f32_e32 v5, v5
	v_mul_f32_e32 v162, v97, v163
	v_add_f32_e32 v163, 1.0, v9
	v_mul_f32_e32 v184, 0x3c000000, v162
	v_mul_f32_e32 v162, v90, v182
	v_rcp_f32_e32 v163, v163
	v_add_f32_e32 v182, 1.0, v156
	v_rcp_f32_e32 v182, v182
	v_mul_f32_e32 v185, 0x3c000000, v162
	v_mul_f32_e32 v162, v91, v163
	v_mul_f32_e32 v186, 0x3c000000, v162
	v_mul_f32_e32 v162, v92, v182
	v_mul_f32_e32 v182, 0x3c000000, v162
	v_add_f32_e32 v162, 1.0, v157
	v_mul_f32_e32 v5, v94, v5
	v_rcp_f32_e32 v187, v162
	v_mul_f32_e32 v5, 0x3c000000, v5
	v_mov_b32_e32 v162, 0
	v_mov_b32_e32 v163, 0
	v_cvt_pk_fp8_f32 v162, v5, v181
	v_cvt_pk_fp8_f32 v163, v185, v186
	v_mul_f32_e32 v5, v93, v187
	v_mul_f32_e32 v5, 0x3c000000, v5
	v_cvt_pk_fp8_f32 v162, v183, v184 op_sel:[0,0,1]
	v_cvt_pk_fp8_f32 v163, v182, v5 op_sel:[0,0,1]
	ds_write_b64 v180, v[162:163] offset:32
	s_cbranch_execz .LBB0_627

; #define LAS __attribute__((address_space(3)))
; __device__ __forceinline__ unsigned pk4_fp8(float a, float b, float c, float d) { int w = 0; w = __builtin_amdgcn_cvt_pk_fp8_f32(a, b, w, false); w = __builtin_amdgcn_cvt_pk_fp8_f32(c, d, w, true); return (unsigned)w; }
; __device__ __forceinline__ float bf_lo(unsigned w) { return __uint_as_float(w << 16); }
; __device__ __forceinline__ float bf_hi(unsigned w) { return __uint_as_float(w & 0xffff0000u); }
; __device__ __forceinline__ float sigmoidf_fast(float x) { return __builtin_amdgcn_rcpf(1.0f + __builtin_amdgcn_exp2f(-1.4426950408889634f * x)); }
;     __device__ __forceinline__ void operator()(f32x4 (&acc)[2][2][4][2], const Unit& u, int wr, int wc, int fr, int fq) const {
;     ...
;             for (int m = 0; m < 4; ++m) {
;                 const size_t ro = (size_t)(u.row0 + ai * 128 + wr * 64 + m * 16 + fr) * DM + col0;
; #pragma unroll
;                 for (int bj = 0; bj < 2; ++bj) {
;                     const u32x4 gd = *(const u32x4*)(GDF + ro + bj * 32);
;                     const float ed[8] = {bf_lo(gd.x), bf_hi(gd.x), bf_lo(gd.y), bf_hi(gd.y), bf_lo(gd.z), bf_hi(gd.z), bf_lo(gd.w), bf_hi(gd.w)};
;                     if (u.tag == 0) {
;                         const u32x4 gn = *(const u32x4*)(GNA + ro + bj * 32);
;                         const float en[8] = {bf_lo(gn.x), bf_hi(gn.x), bf_lo(gn.y), bf_hi(gn.y), bf_lo(gn.z), bf_hi(gn.z), bf_lo(gn.w), bf_hi(gn.w)};
; #pragma unroll
;                         for (int e = 0; e < 8; ++e) {
;                             const float r = (1.0f + __builtin_amdgcn_exp2f(-1.4426950408889634f * ed[e])) * __builtin_amdgcn_rcpf(1.0f + __builtin_amdgcn_exp2f(-1.4426950408889634f * en[e]));
;                             acc[ai][bj][m][e >> 2][e & 3] *= r; }
;                     } else {
;                         float y[8];
; #pragma unroll
;                         for (int e = 0; e < 8; ++e) y[e] = acc[ai][bj][m][e >> 2][e & 3] * sigmoidf_fast(ed[e]) * (PSCALE * WSCALE_INV * OSCALE_INV);
;                         u32x2 w; w.x = pk4_fp8(y[0], y[1], y[2], y[3]); w.y = pk4_fp8(y[4], y[5], y[6], y[7]);
;                         *(LAS u32x2*)(my + fr * 80 + bj * 32 + fq * 8) = w;
.LBB0_577:
	s_nop 1
	v_add_u32_e32 v6, s76, v171
	v_ashrrev_i32_e32 v7, 31, v6
	v_lshlrev_b64 v[6:7], 11, v[6:7]
	v_lshl_add_u64 v[6:7], v[6:7], 0, v[2:3]
	v_lshl_add_u64 v[8:9], v[6:7], 1, s[40:41]
	global_load_dwordx4 v[156:159], v[8:9], off nt
	global_load_dwordx4 v[240:243], v[8:9], off offset:64 nt
	v_lshl_add_u64 v[252:253], v[6:7], 1, s[38:39]
	global_load_dwordx4 v[244:247], v[252:253], off nt
	s_and_b64 vcc, exec, s[4:5]
	s_mov_b64 s[58:59], -1
	s_waitcnt vmcnt(0)
	v_lshlrev_b32_e32 v5, 16, v156
	v_and_b32_e32 v156, 0xffff0000, v156
	v_lshlrev_b32_e32 v160, 16, v157
	v_and_b32_e32 v157, 0xffff0000, v157
	v_lshlrev_b32_e32 v161, 16, v158
	v_and_b32_e32 v158, 0xffff0000, v158
	v_lshlrev_b32_e32 v162, 16, v159
	v_and_b32_e32 v159, 0xffff0000, v159
	v_mul_f32_e32 v5, 0xbfb8aa3b, v5
	v_mul_f32_e32 v156, 0xbfb8aa3b, v156
	v_mul_f32_e32 v163, 0xbfb8aa3b, v160
	v_mul_f32_e32 v157, 0xbfb8aa3b, v157
	v_mul_f32_e32 v181, 0xbfb8aa3b, v161
	v_mul_f32_e32 v158, 0xbfb8aa3b, v158
	v_mul_f32_e32 v182, 0xbfb8aa3b, v162
	v_mul_f32_e32 v159, 0xbfb8aa3b, v159
	v_exp_f32_e32 v160, v5
	v_exp_f32_e32 v161, v156
	v_exp_f32_e32 v162, v163
	v_exp_f32_e32 v163, v157
	v_exp_f32_e32 v156, v181
	v_exp_f32_e32 v157, v158
	v_exp_f32_e32 v158, v182
	v_exp_f32_e32 v159, v159
	s_cbranch_vccnz .LBB0_579
	v_add_f32_e32 v182, 1.0, v162
	v_rcp_f32_e32 v182, v182
	v_add_f32_e32 v183, 1.0, v163
	v_rcp_f32_e32 v183, v183
	v_add_f32_e32 v184, 1.0, v156
	v_rcp_f32_e32 v184, v184
	v_mul_f32_e32 v182, v120, v182
	v_mul_f32_e32 v185, 0x3c000000, v182
	v_mul_f32_e32 v182, v121, v183
	v_add_f32_e32 v183, 1.0, v157
	v_mul_f32_e32 v186, 0x3c000000, v182
	v_mul_f32_e32 v182, v114, v184
	v_rcp_f32_e32 v183, v183
	v_add_f32_e32 v184, 1.0, v158
	v_rcp_f32_e32 v184, v184
	v_add_f32_e32 v5, 1.0, v160
	v_add_f32_e32 v181, 1.0, v161
	v_rcp_f32_e32 v5, v5
	v_rcp_f32_e32 v181, v181
	v_mul_f32_e32 v187, 0x3c000000, v182
	v_mul_f32_e32 v182, v115, v183
	v_mul_f32_e32 v188, 0x3c000000, v182
	v_mul_f32_e32 v182, v116, v184
	v_mul_f32_e32 v184, 0x3c000000, v182
	v_add_f32_e32 v182, 1.0, v159
	v_mul_f32_e32 v5, v118, v5
	v_mul_f32_e32 v181, v119, v181
	v_rcp_f32_e32 v189, v182
	v_mul_f32_e32 v5, 0x3c000000, v5
	v_mul_f32_e32 v181, 0x3c000000, v181
	v_mov_b32_e32 v182, 0
	v_mov_b32_e32 v183, 0
	v_cvt_pk_fp8_f32 v182, v5, v181
	v_cvt_pk_fp8_f32 v183, v187, v188
	v_mul_f32_e32 v5, v117, v189
	v_mul_f32_e32 v5, 0x3c000000, v5
	v_cvt_pk_fp8_f32 v182, v185, v186 op_sel:[0,0,1]
	v_cvt_pk_fp8_f32 v183, v184, v5 op_sel:[0,0,1]
	s_mov_b64 s[58:59], 0
	ds_write_b64 v180, v[182:183]
.LBB0_579:
	s_andn2_b64 vcc, exec, s[58:59]
	v_lshl_add_u64 v[6:7], v[6:7], 1, s[38:39]
	s_cbranch_vccnz .LBB0_581
	v_mov_b64_e32 v[182:183], v[244:245]
	v_mov_b64_e32 v[184:185], v[246:247]
	v_pk_add_f32 v[162:163], v[162:163], 1.0 op_sel_hi:[1,0]
	v_pk_add_f32 v[160:161], v[160:161], 1.0 op_sel_hi:[1,0]
	v_pk_add_f32 v[158:159], v[158:159], 1.0 op_sel_hi:[1,0]
	v_pk_add_f32 v[156:157], v[156:157], 1.0 op_sel_hi:[1,0]
	s_waitcnt vmcnt(0)
	v_lshlrev_b32_e32 v5, 16, v182
	v_and_b32_e32 v181, 0xffff0000, v182
	v_lshlrev_b32_e32 v182, 16, v183
	v_and_b32_e32 v183, 0xffff0000, v183
	v_lshlrev_b32_e32 v186, 16, v184
	v_and_b32_e32 v184, 0xffff0000, v184
	v_lshlrev_b32_e32 v187, 16, v185
	v_and_b32_e32 v185, 0xffff0000, v185
	v_mul_f32_e32 v5, 0xbfb8aa3b, v5
	v_mul_f32_e32 v181, 0xbfb8aa3b, v181
	v_mul_f32_e32 v182, 0xbfb8aa3b, v182
	v_mul_f32_e32 v183, 0xbfb8aa3b, v183
	v_mul_f32_e32 v186, 0xbfb8aa3b, v186
	v_mul_f32_e32 v184, 0xbfb8aa3b, v184
	v_mul_f32_e32 v187, 0xbfb8aa3b, v187
	v_mul_f32_e32 v185, 0xbfb8aa3b, v185
	v_exp_f32_e32 v5, v5
	v_exp_f32_e32 v181, v181
	v_exp_f32_e32 v182, v182
	v_exp_f32_e32 v183, v183
	v_exp_f32_e32 v186, v186
	v_exp_f32_e32 v184, v184
	v_exp_f32_e32 v187, v187
	v_exp_f32_e32 v185, v185
	v_add_f32_e32 v5, 1.0, v5
	v_add_f32_e32 v181, 1.0, v181
	v_add_f32_e32 v188, 1.0, v182
	v_add_f32_e32 v189, 1.0, v183
	v_add_f32_e32 v186, 1.0, v186
	v_add_f32_e32 v190, 1.0, v184
	v_add_f32_e32 v191, 1.0, v187
	v_add_f32_e32 v192, 1.0, v185
	v_rcp_f32_e32 v182, v5
	v_rcp_f32_e32 v183, v181
	v_rcp_f32_e32 v184, v188
	v_rcp_f32_e32 v185, v189
	v_rcp_f32_e32 v186, v186
	v_rcp_f32_e32 v187, v190
	v_rcp_f32_e32 v188, v191
	v_rcp_f32_e32 v189, v192
	v_pk_mul_f32 v[160:161], v[160:161], v[182:183]
	v_pk_mul_f32 v[162:163], v[162:163], v[184:185]
	v_pk_mul_f32 v[156:157], v[156:157], v[186:187]
	v_pk_mul_f32 v[158:159], v[158:159], v[188:189]
	v_pk_mul_f32 v[120:121], v[120:121], v[162:163]
	v_pk_mul_f32 v[118:119], v[118:119], v[160:161]
	v_pk_mul_f32 v[116:117], v[116:117], v[158:159]
	v_pk_mul_f32 v[114:115], v[114:115], v[156:157]
.LBB0_581:
	v_mov_b64_e32 v[156:157], v[240:241]
	v_mov_b64_e32 v[158:159], v[242:243]
	s_and_b64 vcc, exec, s[4:5]
	s_mov_b64 s[58:59], -1
	s_waitcnt vmcnt(0)
	v_lshlrev_b32_e32 v5, 16, v156
	v_and_b32_e32 v8, 0xffff0000, v156
	v_lshlrev_b32_e32 v9, 16, v157
	v_and_b32_e32 v156, 0xffff0000, v157
	v_lshlrev_b32_e32 v157, 16, v158
	v_and_b32_e32 v158, 0xffff0000, v158
	v_lshlrev_b32_e32 v160, 16, v159
	v_and_b32_e32 v159, 0xffff0000, v159
	v_mul_f32_e32 v5, 0xbfb8aa3b, v5
	v_mul_f32_e32 v8, 0xbfb8aa3b, v8
	v_mul_f32_e32 v9, 0xbfb8aa3b, v9
	v_mul_f32_e32 v156, 0xbfb8aa3b, v156
	v_mul_f32_e32 v157, 0xbfb8aa3b, v157
	v_mul_f32_e32 v162, 0xbfb8aa3b, v158
	v_mul_f32_e32 v163, 0xbfb8aa3b, v160
	v_mul_f32_e32 v181, 0xbfb8aa3b, v159
	v_exp_f32_e32 v158, v5
	v_exp_f32_e32 v159, v8
	v_exp_f32_e32 v160, v9
	v_exp_f32_e32 v161, v156
	v_exp_f32_e32 v8, v157
	v_exp_f32_e32 v9, v162
	v_exp_f32_e32 v156, v163
	v_exp_f32_e32 v157, v181
	s_cbranch_vccnz .LBB0_628
	v_add_f32_e32 v162, 1.0, v159
	v_add_f32_e32 v163, 1.0, v160
	v_rcp_f32_e32 v162, v162
	v_rcp_f32_e32 v163, v163
	v_add_f32_e32 v182, 1.0, v8
	v_rcp_f32_e32 v182, v182
	v_mul_f32_e32 v162, v87, v162
	v_mul_f32_e32 v181, 0x3c000000, v162
	v_mul_f32_e32 v162, v88, v163
	v_add_f32_e32 v163, 1.0, v161
	v_rcp_f32_e32 v163, v163
	v_mul_f32_e32 v183, 0x3c000000, v162
	v_add_f32_e32 v5, 1.0, v158
	v_rcp_f32_e32 v5, v5
	v_mul_f32_e32 v162, v89, v163
	v_add_f32_e32 v163, 1.0, v9
	v_mul_f32_e32 v184, 0x3c000000, v162
	v_mul_f32_e32 v162, v82, v182
	v_rcp_f32_e32 v163, v163
	v_add_f32_e32 v182, 1.0, v156
	v_rcp_f32_e32 v182, v182
	v_mul_f32_e32 v185, 0x3c000000, v162
	v_mul_f32_e32 v162, v83, v163
	v_mul_f32_e32 v186, 0x3c000000, v162
	v_mul_f32_e32 v162, v84, v182
	v_mul_f32_e32 v182, 0x3c000000, v162
	v_add_f32_e32 v162, 1.0, v157
	v_mul_f32_e32 v5, v86, v5
	v_rcp_f32_e32 v187, v162
	v_mul_f32_e32 v5, 0x3c000000, v5
	v_mov_b32_e32 v162, 0
	v_mov_b32_e32 v163, 0
	v_cvt_pk_fp8_f32 v162, v5, v181
	v_cvt_pk_fp8_f32 v163, v185, v186
	v_mul_f32_e32 v5, v85, v187
	v_mul_f32_e32 v5, 0x3c000000, v5
	v_cvt_pk_fp8_f32 v162, v183, v184 op_sel:[0,0,1]
	v_cvt_pk_fp8_f32 v163, v182, v5 op_sel:[0,0,1]
	ds_write_b64 v180, v[162:163] offset:32
	s_cbranch_execz .LBB0_629

; #define LAS __attribute__((address_space(3)))
; __device__ __forceinline__ unsigned pk4_fp8(float a, float b, float c, float d) { int w = 0; w = __builtin_amdgcn_cvt_pk_fp8_f32(a, b, w, false); w = __builtin_amdgcn_cvt_pk_fp8_f32(c, d, w, true); return (unsigned)w; }
; __device__ __forceinline__ float bf_lo(unsigned w) { return __uint_as_float(w << 16); }
; __device__ __forceinline__ float bf_hi(unsigned w) { return __uint_as_float(w & 0xffff0000u); }
; __device__ __forceinline__ float sigmoidf_fast(float x) { return __builtin_amdgcn_rcpf(1.0f + __builtin_amdgcn_exp2f(-1.4426950408889634f * x)); }
;     __device__ __forceinline__ void operator()(f32x4 (&acc)[2][2][4][2], const Unit& u, int wr, int wc, int fr, int fq) const {
;     ...
;             for (int m = 0; m < 4; ++m) {
;                 const size_t ro = (size_t)(u.row0 + ai * 128 + wr * 64 + m * 16 + fr) * DM + col0;
; #pragma unroll
;                 for (int bj = 0; bj < 2; ++bj) {
;                     const u32x4 gd = *(const u32x4*)(GDF + ro + bj * 32);
;                     const float ed[8] = {bf_lo(gd.x), bf_hi(gd.x), bf_lo(gd.y), bf_hi(gd.y), bf_lo(gd.z), bf_hi(gd.z), bf_lo(gd.w), bf_hi(gd.w)};
;                     if (u.tag == 0) {
;                         const u32x4 gn = *(const u32x4*)(GNA + ro + bj * 32);
;                         const float en[8] = {bf_lo(gn.x), bf_hi(gn.x), bf_lo(gn.y), bf_hi(gn.y), bf_lo(gn.z), bf_hi(gn.z), bf_lo(gn.w), bf_hi(gn.w)};
; #pragma unroll
;                         for (int e = 0; e < 8; ++e) {
;                             const float r = (1.0f + __builtin_amdgcn_exp2f(-1.4426950408889634f * ed[e])) * __builtin_amdgcn_rcpf(1.0f + __builtin_amdgcn_exp2f(-1.4426950408889634f * en[e]));
;                             acc[ai][bj][m][e >> 2][e & 3] *= r; }
;                     } else {
;                         float y[8];
; #pragma unroll
;                         for (int e = 0; e < 8; ++e) y[e] = acc[ai][bj][m][e >> 2][e & 3] * sigmoidf_fast(ed[e]) * (PSCALE * WSCALE_INV * OSCALE_INV);
;                         u32x2 w; w.x = pk4_fp8(y[0], y[1], y[2], y[3]); w.y = pk4_fp8(y[4], y[5], y[6], y[7]);
;                         *(LAS u32x2*)(my + fr * 80 + bj * 32 + fq * 8) = w;
.LBB0_585:
	s_nop 1
	v_add_u32_e32 v6, s76, v173
	v_ashrrev_i32_e32 v7, 31, v6
	v_lshlrev_b64 v[6:7], 11, v[6:7]
	v_lshl_add_u64 v[6:7], v[6:7], 0, v[2:3]
	v_lshl_add_u64 v[8:9], v[6:7], 1, s[40:41]
	global_load_dwordx4 v[156:159], v[8:9], off nt
	global_load_dwordx4 v[240:243], v[8:9], off offset:64 nt
	v_lshl_add_u64 v[252:253], v[6:7], 1, s[38:39]
	global_load_dwordx4 v[244:247], v[252:253], off nt
	s_and_b64 vcc, exec, s[4:5]
	s_mov_b64 s[58:59], -1
	s_waitcnt vmcnt(0)
	v_lshlrev_b32_e32 v5, 16, v156
	v_and_b32_e32 v156, 0xffff0000, v156
	v_lshlrev_b32_e32 v160, 16, v157
	v_and_b32_e32 v157, 0xffff0000, v157
	v_lshlrev_b32_e32 v161, 16, v158
	v_and_b32_e32 v158, 0xffff0000, v158
	v_lshlrev_b32_e32 v162, 16, v159
	v_and_b32_e32 v159, 0xffff0000, v159
	v_mul_f32_e32 v5, 0xbfb8aa3b, v5
	v_mul_f32_e32 v156, 0xbfb8aa3b, v156
	v_mul_f32_e32 v163, 0xbfb8aa3b, v160
	v_mul_f32_e32 v157, 0xbfb8aa3b, v157
	v_mul_f32_e32 v181, 0xbfb8aa3b, v161
	v_mul_f32_e32 v158, 0xbfb8aa3b, v158
	v_mul_f32_e32 v182, 0xbfb8aa3b, v162
	v_mul_f32_e32 v159, 0xbfb8aa3b, v159
	v_exp_f32_e32 v160, v5
	v_exp_f32_e32 v161, v156
	v_exp_f32_e32 v162, v163
	v_exp_f32_e32 v163, v157
	v_exp_f32_e32 v156, v181
	v_exp_f32_e32 v157, v158
	v_exp_f32_e32 v158, v182
	v_exp_f32_e32 v159, v159
	s_cbranch_vccnz .LBB0_587
	v_add_f32_e32 v182, 1.0, v162
	v_rcp_f32_e32 v182, v182
	v_add_f32_e32 v183, 1.0, v163
	v_rcp_f32_e32 v183, v183
	v_add_f32_e32 v184, 1.0, v156
	v_rcp_f32_e32 v184, v184
	v_mul_f32_e32 v182, v112, v182
	v_mul_f32_e32 v185, 0x3c000000, v182
	v_mul_f32_e32 v182, v113, v183
	v_add_f32_e32 v183, 1.0, v157
	v_mul_f32_e32 v186, 0x3c000000, v182
	v_mul_f32_e32 v182, v106, v184
	v_rcp_f32_e32 v183, v183
	v_add_f32_e32 v184, 1.0, v158
	v_rcp_f32_e32 v184, v184
	v_add_f32_e32 v5, 1.0, v160
	v_add_f32_e32 v181, 1.0, v161
	v_rcp_f32_e32 v5, v5
	v_rcp_f32_e32 v181, v181
	v_mul_f32_e32 v187, 0x3c000000, v182
	v_mul_f32_e32 v182, v107, v183
	v_mul_f32_e32 v188, 0x3c000000, v182
	v_mul_f32_e32 v182, v108, v184
	v_mul_f32_e32 v184, 0x3c000000, v182
	v_add_f32_e32 v182, 1.0, v159
	v_mul_f32_e32 v5, v110, v5
	v_mul_f32_e32 v181, v111, v181
	v_rcp_f32_e32 v189, v182
	v_mul_f32_e32 v5, 0x3c000000, v5
	v_mul_f32_e32 v181, 0x3c000000, v181
	v_mov_b32_e32 v182, 0
	v_mov_b32_e32 v183, 0
	v_cvt_pk_fp8_f32 v182, v5, v181
	v_cvt_pk_fp8_f32 v183, v187, v188
	v_mul_f32_e32 v5, v109, v189
	v_mul_f32_e32 v5, 0x3c000000, v5
	v_cvt_pk_fp8_f32 v182, v185, v186 op_sel:[0,0,1]
	v_cvt_pk_fp8_f32 v183, v184, v5 op_sel:[0,0,1]
	s_mov_b64 s[58:59], 0
	ds_write_b64 v180, v[182:183]
.LBB0_587:
	s_andn2_b64 vcc, exec, s[58:59]
	v_lshl_add_u64 v[6:7], v[6:7], 1, s[38:39]
	s_cbranch_vccnz .LBB0_589
	v_mov_b64_e32 v[182:183], v[244:245]
	v_mov_b64_e32 v[184:185], v[246:247]
	v_pk_add_f32 v[162:163], v[162:163], 1.0 op_sel_hi:[1,0]
	v_pk_add_f32 v[160:161], v[160:161], 1.0 op_sel_hi:[1,0]
	v_pk_add_f32 v[158:159], v[158:159], 1.0 op_sel_hi:[1,0]
	v_pk_add_f32 v[156:157], v[156:157], 1.0 op_sel_hi:[1,0]
	s_waitcnt vmcnt(0)
	v_lshlrev_b32_e32 v5, 16, v182
	v_and_b32_e32 v181, 0xffff0000, v182
	v_lshlrev_b32_e32 v182, 16, v183
	v_and_b32_e32 v183, 0xffff0000, v183
	v_lshlrev_b32_e32 v186, 16, v184
	v_and_b32_e32 v184, 0xffff0000, v184
	v_lshlrev_b32_e32 v187, 16, v185
	v_and_b32_e32 v185, 0xffff0000, v185
	v_mul_f32_e32 v5, 0xbfb8aa3b, v5
	v_mul_f32_e32 v181, 0xbfb8aa3b, v181
	v_mul_f32_e32 v182, 0xbfb8aa3b, v182
	v_mul_f32_e32 v183, 0xbfb8aa3b, v183
	v_mul_f32_e32 v186, 0xbfb8aa3b, v186
	v_mul_f32_e32 v184, 0xbfb8aa3b, v184
	v_mul_f32_e32 v187, 0xbfb8aa3b, v187
	v_mul_f32_e32 v185, 0xbfb8aa3b, v185
	v_exp_f32_e32 v5, v5
	v_exp_f32_e32 v181, v181
	v_exp_f32_e32 v182, v182
	v_exp_f32_e32 v183, v183
	v_exp_f32_e32 v186, v186
	v_exp_f32_e32 v184, v184
	v_exp_f32_e32 v187, v187
	v_exp_f32_e32 v185, v185
	v_add_f32_e32 v5, 1.0, v5
	v_add_f32_e32 v181, 1.0, v181
	v_add_f32_e32 v188, 1.0, v182
	v_add_f32_e32 v189, 1.0, v183
	v_add_f32_e32 v186, 1.0, v186
	v_add_f32_e32 v190, 1.0, v184
	v_add_f32_e32 v191, 1.0, v187
	v_add_f32_e32 v192, 1.0, v185
	v_rcp_f32_e32 v182, v5
	v_rcp_f32_e32 v183, v181
	v_rcp_f32_e32 v184, v188
	v_rcp_f32_e32 v185, v189
	v_rcp_f32_e32 v186, v186
	v_rcp_f32_e32 v187, v190
	v_rcp_f32_e32 v188, v191
	v_rcp_f32_e32 v189, v192
	v_pk_mul_f32 v[160:161], v[160:161], v[182:183]
	v_pk_mul_f32 v[162:163], v[162:163], v[184:185]
	v_pk_mul_f32 v[156:157], v[156:157], v[186:187]
	v_pk_mul_f32 v[158:159], v[158:159], v[188:189]
	v_pk_mul_f32 v[112:113], v[112:113], v[162:163]
	v_pk_mul_f32 v[110:111], v[110:111], v[160:161]
	v_pk_mul_f32 v[108:109], v[108:109], v[158:159]
	v_pk_mul_f32 v[106:107], v[106:107], v[156:157]
.LBB0_589:
	v_mov_b64_e32 v[156:157], v[240:241]
	v_mov_b64_e32 v[158:159], v[242:243]
	s_and_b64 vcc, exec, s[4:5]
	s_mov_b64 s[58:59], -1
	s_waitcnt vmcnt(0)
	v_lshlrev_b32_e32 v5, 16, v156
	v_and_b32_e32 v8, 0xffff0000, v156
	v_lshlrev_b32_e32 v9, 16, v157
	v_and_b32_e32 v156, 0xffff0000, v157
	v_lshlrev_b32_e32 v157, 16, v158
	v_and_b32_e32 v158, 0xffff0000, v158
	v_lshlrev_b32_e32 v160, 16, v159
	v_and_b32_e32 v159, 0xffff0000, v159
	v_mul_f32_e32 v5, 0xbfb8aa3b, v5
	v_mul_f32_e32 v8, 0xbfb8aa3b, v8
	v_mul_f32_e32 v9, 0xbfb8aa3b, v9
	v_mul_f32_e32 v156, 0xbfb8aa3b, v156
	v_mul_f32_e32 v157, 0xbfb8aa3b, v157
	v_mul_f32_e32 v162, 0xbfb8aa3b, v158
	v_mul_f32_e32 v163, 0xbfb8aa3b, v160
	v_mul_f32_e32 v181, 0xbfb8aa3b, v159
	v_exp_f32_e32 v158, v5
	v_exp_f32_e32 v159, v8
	v_exp_f32_e32 v160, v9
	v_exp_f32_e32 v161, v156
	v_exp_f32_e32 v8, v157
	v_exp_f32_e32 v9, v162
	v_exp_f32_e32 v156, v163
	v_exp_f32_e32 v157, v181
	s_cbranch_vccnz .LBB0_630
	v_add_f32_e32 v162, 1.0, v159
	v_add_f32_e32 v163, 1.0, v160
	v_rcp_f32_e32 v162, v162
	v_rcp_f32_e32 v163, v163
	v_add_f32_e32 v182, 1.0, v8
	v_rcp_f32_e32 v182, v182
	v_mul_f32_e32 v162, v79, v162
	v_mul_f32_e32 v181, 0x3c000000, v162
	v_mul_f32_e32 v162, v80, v163
	v_add_f32_e32 v163, 1.0, v161
	v_rcp_f32_e32 v163, v163
	v_mul_f32_e32 v183, 0x3c000000, v162
	v_add_f32_e32 v5, 1.0, v158
	v_rcp_f32_e32 v5, v5
	v_mul_f32_e32 v162, v81, v163
	v_add_f32_e32 v163, 1.0, v9
	v_mul_f32_e32 v184, 0x3c000000, v162
	v_mul_f32_e32 v162, v74, v182
	v_rcp_f32_e32 v163, v163
	v_add_f32_e32 v182, 1.0, v156
	v_rcp_f32_e32 v182, v182
	v_mul_f32_e32 v185, 0x3c000000, v162
	v_mul_f32_e32 v162, v75, v163
	v_mul_f32_e32 v186, 0x3c000000, v162
	v_mul_f32_e32 v162, v76, v182
	v_mul_f32_e32 v182, 0x3c000000, v162
	v_add_f32_e32 v162, 1.0, v157
	v_mul_f32_e32 v5, v78, v5
	v_rcp_f32_e32 v187, v162
	v_mul_f32_e32 v5, 0x3c000000, v5
	v_mov_b32_e32 v162, 0
	v_mov_b32_e32 v163, 0
	v_cvt_pk_fp8_f32 v162, v5, v181
	v_cvt_pk_fp8_f32 v163, v185, v186
	v_mul_f32_e32 v5, v77, v187
	v_mul_f32_e32 v5, 0x3c000000, v5
	v_cvt_pk_fp8_f32 v162, v183, v184 op_sel:[0,0,1]
	v_cvt_pk_fp8_f32 v163, v182, v5 op_sel:[0,0,1]
	ds_write_b64 v180, v[162:163] offset:32
	s_cbranch_execz .LBB0_631

; #define LAS __attribute__((address_space(3)))
; __device__ __forceinline__ unsigned pk4_fp8(float a, float b, float c, float d) { int w = 0; w = __builtin_amdgcn_cvt_pk_fp8_f32(a, b, w, false); w = __builtin_amdgcn_cvt_pk_fp8_f32(c, d, w, true); return (unsigned)w; }
; __device__ __forceinline__ float bf_lo(unsigned w) { return __uint_as_float(w << 16); }
; __device__ __forceinline__ float bf_hi(unsigned w) { return __uint_as_float(w & 0xffff0000u); }
; __device__ __forceinline__ float sigmoidf_fast(float x) { return __builtin_amdgcn_rcpf(1.0f + __builtin_amdgcn_exp2f(-1.4426950408889634f * x)); }
;     __device__ __forceinline__ void operator()(f32x4 (&acc)[2][2][4][2], const Unit& u, int wr, int wc, int fr, int fq) const {
;     ...
;             for (int m = 0; m < 4; ++m) {
;                 const size_t ro = (size_t)(u.row0 + ai * 128 + wr * 64 + m * 16 + fr) * DM + col0;
; #pragma unroll
;                 for (int bj = 0; bj < 2; ++bj) {
;                     const u32x4 gd = *(const u32x4*)(GDF + ro + bj * 32);
;                     const float ed[8] = {bf_lo(gd.x), bf_hi(gd.x), bf_lo(gd.y), bf_hi(gd.y), bf_lo(gd.z), bf_hi(gd.z), bf_lo(gd.w), bf_hi(gd.w)};
;                     if (u.tag == 0) {
;                         const u32x4 gn = *(const u32x4*)(GNA + ro + bj * 32);
;                         const float en[8] = {bf_lo(gn.x), bf_hi(gn.x), bf_lo(gn.y), bf_hi(gn.y), bf_lo(gn.z), bf_hi(gn.z), bf_lo(gn.w), bf_hi(gn.w)};
; #pragma unroll
;                         for (int e = 0; e < 8; ++e) {
;                             const float r = (1.0f + __builtin_amdgcn_exp2f(-1.4426950408889634f * ed[e])) * __builtin_amdgcn_rcpf(1.0f + __builtin_amdgcn_exp2f(-1.4426950408889634f * en[e]));
;                             acc[ai][bj][m][e >> 2][e & 3] *= r; }
;                     } else {
;                         float y[8];
; #pragma unroll
;                         for (int e = 0; e < 8; ++e) y[e] = acc[ai][bj][m][e >> 2][e & 3] * sigmoidf_fast(ed[e]) * (PSCALE * WSCALE_INV * OSCALE_INV);
;                         u32x2 w; w.x = pk4_fp8(y[0], y[1], y[2], y[3]); w.y = pk4_fp8(y[4], y[5], y[6], y[7]);
;                         *(LAS u32x2*)(my + fr * 80 + bj * 32 + fq * 8) = w;
.LBB0_593:
	s_nop 1
	v_add_u32_e32 v6, 0x80, v4
	v_ashrrev_i32_e32 v7, 31, v6
	v_lshlrev_b64 v[6:7], 11, v[6:7]
	v_lshl_add_u64 v[6:7], v[6:7], 0, v[2:3]
	v_lshl_add_u64 v[8:9], v[6:7], 1, s[40:41]
	global_load_dwordx4 v[156:159], v[8:9], off nt
	global_load_dwordx4 v[240:243], v[8:9], off offset:64 nt
	v_lshl_add_u64 v[252:253], v[6:7], 1, s[38:39]
	global_load_dwordx4 v[244:247], v[252:253], off nt
	s_and_b64 vcc, exec, s[4:5]
	s_mov_b64 s[58:59], -1
	s_waitcnt vmcnt(0)
	v_lshlrev_b32_e32 v5, 16, v156
	v_and_b32_e32 v156, 0xffff0000, v156
	v_lshlrev_b32_e32 v160, 16, v157
	v_and_b32_e32 v157, 0xffff0000, v157
	v_lshlrev_b32_e32 v161, 16, v158
	v_and_b32_e32 v158, 0xffff0000, v158
	v_lshlrev_b32_e32 v162, 16, v159
	v_and_b32_e32 v159, 0xffff0000, v159
	v_mul_f32_e32 v5, 0xbfb8aa3b, v5
	v_mul_f32_e32 v156, 0xbfb8aa3b, v156
	v_mul_f32_e32 v163, 0xbfb8aa3b, v160
	v_mul_f32_e32 v157, 0xbfb8aa3b, v157
	v_mul_f32_e32 v181, 0xbfb8aa3b, v161
	v_mul_f32_e32 v158, 0xbfb8aa3b, v158
	v_mul_f32_e32 v182, 0xbfb8aa3b, v162
	v_mul_f32_e32 v159, 0xbfb8aa3b, v159
	v_exp_f32_e32 v160, v5
	v_exp_f32_e32 v161, v156
	v_exp_f32_e32 v162, v163
	v_exp_f32_e32 v163, v157
	v_exp_f32_e32 v156, v181
	v_exp_f32_e32 v157, v158
	v_exp_f32_e32 v158, v182
	v_exp_f32_e32 v159, v159
	s_cbranch_vccnz .LBB0_595
	v_add_f32_e32 v182, 1.0, v162
	v_rcp_f32_e32 v182, v182
	v_add_f32_e32 v183, 1.0, v163
	v_rcp_f32_e32 v183, v183
	v_add_f32_e32 v184, 1.0, v156
	v_rcp_f32_e32 v184, v184
	v_mul_f32_e32 v182, v72, v182
	v_mul_f32_e32 v185, 0x3c000000, v182
	v_mul_f32_e32 v182, v73, v183
	v_add_f32_e32 v183, 1.0, v157
	v_mul_f32_e32 v186, 0x3c000000, v182
	v_mul_f32_e32 v182, v66, v184
	v_rcp_f32_e32 v183, v183
	v_add_f32_e32 v184, 1.0, v158
	v_rcp_f32_e32 v184, v184
	v_add_f32_e32 v5, 1.0, v160
	v_add_f32_e32 v181, 1.0, v161
	v_rcp_f32_e32 v5, v5
	v_rcp_f32_e32 v181, v181
	v_mul_f32_e32 v187, 0x3c000000, v182
	v_mul_f32_e32 v182, v67, v183
	v_mul_f32_e32 v188, 0x3c000000, v182
	v_mul_f32_e32 v182, v68, v184
	v_mul_f32_e32 v184, 0x3c000000, v182
	v_add_f32_e32 v182, 1.0, v159
	v_mul_f32_e32 v5, v70, v5
	v_mul_f32_e32 v181, v71, v181
	v_rcp_f32_e32 v189, v182
	v_mul_f32_e32 v5, 0x3c000000, v5
	v_mul_f32_e32 v181, 0x3c000000, v181
	v_mov_b32_e32 v182, 0
	v_mov_b32_e32 v183, 0
	v_cvt_pk_fp8_f32 v182, v5, v181
	v_cvt_pk_fp8_f32 v183, v187, v188
	v_mul_f32_e32 v5, v69, v189
	v_mul_f32_e32 v5, 0x3c000000, v5
	v_cvt_pk_fp8_f32 v182, v185, v186 op_sel:[0,0,1]
	v_cvt_pk_fp8_f32 v183, v184, v5 op_sel:[0,0,1]
	s_mov_b64 s[58:59], 0
	ds_write_b64 v180, v[182:183]
.LBB0_595:
	s_andn2_b64 vcc, exec, s[58:59]
	v_lshl_add_u64 v[6:7], v[6:7], 1, s[38:39]
	s_cbranch_vccnz .LBB0_597
	v_mov_b64_e32 v[182:183], v[244:245]
	v_mov_b64_e32 v[184:185], v[246:247]
	v_pk_add_f32 v[162:163], v[162:163], 1.0 op_sel_hi:[1,0]
	v_pk_add_f32 v[160:161], v[160:161], 1.0 op_sel_hi:[1,0]
	v_pk_add_f32 v[158:159], v[158:159], 1.0 op_sel_hi:[1,0]
	v_pk_add_f32 v[156:157], v[156:157], 1.0 op_sel_hi:[1,0]
	s_waitcnt vmcnt(0)
	v_lshlrev_b32_e32 v5, 16, v182
	v_and_b32_e32 v181, 0xffff0000, v182
	v_lshlrev_b32_e32 v182, 16, v183
	v_and_b32_e32 v183, 0xffff0000, v183
	v_lshlrev_b32_e32 v186, 16, v184
	v_and_b32_e32 v184, 0xffff0000, v184
	v_lshlrev_b32_e32 v187, 16, v185
	v_and_b32_e32 v185, 0xffff0000, v185
	v_mul_f32_e32 v5, 0xbfb8aa3b, v5
	v_mul_f32_e32 v181, 0xbfb8aa3b, v181
	v_mul_f32_e32 v182, 0xbfb8aa3b, v182
	v_mul_f32_e32 v183, 0xbfb8aa3b, v183
	v_mul_f32_e32 v186, 0xbfb8aa3b, v186
	v_mul_f32_e32 v184, 0xbfb8aa3b, v184
	v_mul_f32_e32 v187, 0xbfb8aa3b, v187
	v_mul_f32_e32 v185, 0xbfb8aa3b, v185
	v_exp_f32_e32 v5, v5
	v_exp_f32_e32 v181, v181
	v_exp_f32_e32 v182, v182
	v_exp_f32_e32 v183, v183
	v_exp_f32_e32 v186, v186
	v_exp_f32_e32 v184, v184
	v_exp_f32_e32 v187, v187
	v_exp_f32_e32 v185, v185
	v_add_f32_e32 v5, 1.0, v5
	v_add_f32_e32 v181, 1.0, v181
	v_add_f32_e32 v188, 1.0, v182
	v_add_f32_e32 v189, 1.0, v183
	v_add_f32_e32 v186, 1.0, v186
	v_add_f32_e32 v190, 1.0, v184
	v_add_f32_e32 v191, 1.0, v187
	v_add_f32_e32 v192, 1.0, v185
	v_rcp_f32_e32 v182, v5
	v_rcp_f32_e32 v183, v181
	v_rcp_f32_e32 v184, v188
	v_rcp_f32_e32 v185, v189
	v_rcp_f32_e32 v186, v186
	v_rcp_f32_e32 v187, v190
	v_rcp_f32_e32 v188, v191
	v_rcp_f32_e32 v189, v192
	v_pk_mul_f32 v[160:161], v[160:161], v[182:183]
	v_pk_mul_f32 v[162:163], v[162:163], v[184:185]
	v_pk_mul_f32 v[156:157], v[156:157], v[186:187]
	v_pk_mul_f32 v[158:159], v[158:159], v[188:189]
	v_pk_mul_f32 v[72:73], v[72:73], v[162:163]
	v_pk_mul_f32 v[70:71], v[70:71], v[160:161]
	v_pk_mul_f32 v[68:69], v[68:69], v[158:159]
	v_pk_mul_f32 v[66:67], v[66:67], v[156:157]
.LBB0_597:
	v_mov_b64_e32 v[156:157], v[240:241]
	v_mov_b64_e32 v[158:159], v[242:243]
	s_and_b64 vcc, exec, s[4:5]
	s_mov_b64 s[58:59], -1
	s_waitcnt vmcnt(0)
	v_lshlrev_b32_e32 v5, 16, v156
	v_and_b32_e32 v8, 0xffff0000, v156
	v_lshlrev_b32_e32 v9, 16, v157
	v_and_b32_e32 v156, 0xffff0000, v157
	v_lshlrev_b32_e32 v157, 16, v158
	v_and_b32_e32 v158, 0xffff0000, v158
	v_lshlrev_b32_e32 v160, 16, v159
	v_and_b32_e32 v159, 0xffff0000, v159
	v_mul_f32_e32 v5, 0xbfb8aa3b, v5
	v_mul_f32_e32 v8, 0xbfb8aa3b, v8
	v_mul_f32_e32 v9, 0xbfb8aa3b, v9
	v_mul_f32_e32 v156, 0xbfb8aa3b, v156
	v_mul_f32_e32 v157, 0xbfb8aa3b, v157
	v_mul_f32_e32 v162, 0xbfb8aa3b, v158
	v_mul_f32_e32 v163, 0xbfb8aa3b, v160
	v_mul_f32_e32 v181, 0xbfb8aa3b, v159
	v_exp_f32_e32 v158, v5
	v_exp_f32_e32 v159, v8
	v_exp_f32_e32 v160, v9
	v_exp_f32_e32 v161, v156
	v_exp_f32_e32 v8, v157
	v_exp_f32_e32 v9, v162
	v_exp_f32_e32 v156, v163
	v_exp_f32_e32 v157, v181
	s_cbranch_vccnz .LBB0_632
	v_add_f32_e32 v162, 1.0, v159
	v_add_f32_e32 v163, 1.0, v160
	v_rcp_f32_e32 v162, v162
	v_rcp_f32_e32 v163, v163
	v_add_f32_e32 v182, 1.0, v8
	v_rcp_f32_e32 v182, v182
	v_mul_f32_e32 v162, v39, v162
	v_mul_f32_e32 v181, 0x3c000000, v162
	v_mul_f32_e32 v162, v40, v163
	v_add_f32_e32 v163, 1.0, v161
	v_rcp_f32_e32 v163, v163
	v_mul_f32_e32 v183, 0x3c000000, v162
	v_add_f32_e32 v5, 1.0, v158
	v_rcp_f32_e32 v5, v5
	v_mul_f32_e32 v162, v41, v163
	v_add_f32_e32 v163, 1.0, v9
	v_mul_f32_e32 v184, 0x3c000000, v162
	v_mul_f32_e32 v162, v34, v182
	v_rcp_f32_e32 v163, v163
	v_add_f32_e32 v182, 1.0, v156
	v_rcp_f32_e32 v182, v182
	v_mul_f32_e32 v185, 0x3c000000, v162
	v_mul_f32_e32 v162, v35, v163
	v_mul_f32_e32 v186, 0x3c000000, v162
	v_mul_f32_e32 v162, v36, v182
	v_mul_f32_e32 v182, 0x3c000000, v162
	v_add_f32_e32 v162, 1.0, v157
	v_mul_f32_e32 v5, v38, v5
	v_rcp_f32_e32 v187, v162
	v_mul_f32_e32 v5, 0x3c000000, v5
	v_mov_b32_e32 v162, 0
	v_mov_b32_e32 v163, 0
	v_cvt_pk_fp8_f32 v162, v5, v181
	v_cvt_pk_fp8_f32 v163, v185, v186
	v_mul_f32_e32 v5, v37, v187
	v_mul_f32_e32 v5, 0x3c000000, v5
	v_cvt_pk_fp8_f32 v162, v183, v184 op_sel:[0,0,1]
	v_cvt_pk_fp8_f32 v163, v182, v5 op_sel:[0,0,1]
	ds_write_b64 v180, v[162:163] offset:32
	s_cbranch_execz .LBB0_633

; #define LAS __attribute__((address_space(3)))
; __device__ __forceinline__ unsigned pk4_fp8(float a, float b, float c, float d) { int w = 0; w = __builtin_amdgcn_cvt_pk_fp8_f32(a, b, w, false); w = __builtin_amdgcn_cvt_pk_fp8_f32(c, d, w, true); return (unsigned)w; }
; __device__ __forceinline__ float bf_lo(unsigned w) { return __uint_as_float(w << 16); }
; __device__ __forceinline__ float bf_hi(unsigned w) { return __uint_as_float(w & 0xffff0000u); }
; __device__ __forceinline__ float sigmoidf_fast(float x) { return __builtin_amdgcn_rcpf(1.0f + __builtin_amdgcn_exp2f(-1.4426950408889634f * x)); }
;     __device__ __forceinline__ void operator()(f32x4 (&acc)[2][2][4][2], const Unit& u, int wr, int wc, int fr, int fq) const {
;     ...
;             for (int m = 0; m < 4; ++m) {
;                 const size_t ro = (size_t)(u.row0 + ai * 128 + wr * 64 + m * 16 + fr) * DM + col0;
; #pragma unroll
;                 for (int bj = 0; bj < 2; ++bj) {
;                     const u32x4 gd = *(const u32x4*)(GDF + ro + bj * 32);
;                     const float ed[8] = {bf_lo(gd.x), bf_hi(gd.x), bf_lo(gd.y), bf_hi(gd.y), bf_lo(gd.z), bf_hi(gd.z), bf_lo(gd.w), bf_hi(gd.w)};
;                     if (u.tag == 0) {
;                         const u32x4 gn = *(const u32x4*)(GNA + ro + bj * 32);
;                         const float en[8] = {bf_lo(gn.x), bf_hi(gn.x), bf_lo(gn.y), bf_hi(gn.y), bf_lo(gn.z), bf_hi(gn.z), bf_lo(gn.w), bf_hi(gn.w)};
; #pragma unroll
;                         for (int e = 0; e < 8; ++e) {
;                             const float r = (1.0f + __builtin_amdgcn_exp2f(-1.4426950408889634f * ed[e])) * __builtin_amdgcn_rcpf(1.0f + __builtin_amdgcn_exp2f(-1.4426950408889634f * en[e]));
;                             acc[ai][bj][m][e >> 2][e & 3] *= r; }
;                     } else {
;                         float y[8];
; #pragma unroll
;                         for (int e = 0; e < 8; ++e) y[e] = acc[ai][bj][m][e >> 2][e & 3] * sigmoidf_fast(ed[e]) * (PSCALE * WSCALE_INV * OSCALE_INV);
;                         u32x2 w; w.x = pk4_fp8(y[0], y[1], y[2], y[3]); w.y = pk4_fp8(y[4], y[5], y[6], y[7]);
;                         *(LAS u32x2*)(my + fr * 80 + bj * 32 + fq * 8) = w;
.LBB0_601:
	s_nop 1
	v_add_u32_e32 v6, 0x90, v4
	v_ashrrev_i32_e32 v7, 31, v6
	v_lshlrev_b64 v[6:7], 11, v[6:7]
	v_lshl_add_u64 v[6:7], v[6:7], 0, v[2:3]
	v_lshl_add_u64 v[8:9], v[6:7], 1, s[40:41]
	global_load_dwordx4 v[156:159], v[8:9], off nt
	global_load_dwordx4 v[240:243], v[8:9], off offset:64 nt
	v_lshl_add_u64 v[252:253], v[6:7], 1, s[38:39]
	global_load_dwordx4 v[244:247], v[252:253], off nt
	s_and_b64 vcc, exec, s[4:5]
	s_mov_b64 s[58:59], -1
	s_waitcnt vmcnt(0)
	v_lshlrev_b32_e32 v5, 16, v156
	v_and_b32_e32 v156, 0xffff0000, v156
	v_lshlrev_b32_e32 v160, 16, v157
	v_and_b32_e32 v157, 0xffff0000, v157
	v_lshlrev_b32_e32 v161, 16, v158
	v_and_b32_e32 v158, 0xffff0000, v158
	v_lshlrev_b32_e32 v162, 16, v159
	v_and_b32_e32 v159, 0xffff0000, v159
	v_mul_f32_e32 v5, 0xbfb8aa3b, v5
	v_mul_f32_e32 v156, 0xbfb8aa3b, v156
	v_mul_f32_e32 v163, 0xbfb8aa3b, v160
	v_mul_f32_e32 v157, 0xbfb8aa3b, v157
	v_mul_f32_e32 v181, 0xbfb8aa3b, v161
	v_mul_f32_e32 v158, 0xbfb8aa3b, v158
	v_mul_f32_e32 v182, 0xbfb8aa3b, v162
	v_mul_f32_e32 v159, 0xbfb8aa3b, v159
	v_exp_f32_e32 v160, v5
	v_exp_f32_e32 v161, v156
	v_exp_f32_e32 v162, v163
	v_exp_f32_e32 v163, v157
	v_exp_f32_e32 v156, v181
	v_exp_f32_e32 v157, v158
	v_exp_f32_e32 v158, v182
	v_exp_f32_e32 v159, v159
	s_cbranch_vccnz .LBB0_603
	v_add_f32_e32 v182, 1.0, v162
	v_rcp_f32_e32 v182, v182
	v_add_f32_e32 v183, 1.0, v163
	v_rcp_f32_e32 v183, v183
	v_add_f32_e32 v184, 1.0, v156
	v_rcp_f32_e32 v184, v184
	v_mul_f32_e32 v182, v64, v182
	v_mul_f32_e32 v185, 0x3c000000, v182
	v_mul_f32_e32 v182, v65, v183
	v_add_f32_e32 v183, 1.0, v157
	v_mul_f32_e32 v186, 0x3c000000, v182
	v_mul_f32_e32 v182, v58, v184
	v_rcp_f32_e32 v183, v183
	v_add_f32_e32 v184, 1.0, v158
	v_rcp_f32_e32 v184, v184
	v_add_f32_e32 v5, 1.0, v160
	v_add_f32_e32 v181, 1.0, v161
	v_rcp_f32_e32 v5, v5
	v_rcp_f32_e32 v181, v181
	v_mul_f32_e32 v187, 0x3c000000, v182
	v_mul_f32_e32 v182, v59, v183
	v_mul_f32_e32 v188, 0x3c000000, v182
	v_mul_f32_e32 v182, v60, v184
	v_mul_f32_e32 v184, 0x3c000000, v182
	v_add_f32_e32 v182, 1.0, v159
	v_mul_f32_e32 v5, v62, v5
	v_mul_f32_e32 v181, v63, v181
	v_rcp_f32_e32 v189, v182
	v_mul_f32_e32 v5, 0x3c000000, v5
	v_mul_f32_e32 v181, 0x3c000000, v181
	v_mov_b32_e32 v182, 0
	v_mov_b32_e32 v183, 0
	v_cvt_pk_fp8_f32 v182, v5, v181
	v_cvt_pk_fp8_f32 v183, v187, v188
	v_mul_f32_e32 v5, v61, v189
	v_mul_f32_e32 v5, 0x3c000000, v5
	v_cvt_pk_fp8_f32 v182, v185, v186 op_sel:[0,0,1]
	v_cvt_pk_fp8_f32 v183, v184, v5 op_sel:[0,0,1]
	s_mov_b64 s[58:59], 0
	ds_write_b64 v180, v[182:183]
.LBB0_603:
	s_andn2_b64 vcc, exec, s[58:59]
	v_lshl_add_u64 v[6:7], v[6:7], 1, s[38:39]
	s_cbranch_vccnz .LBB0_605
	v_mov_b64_e32 v[182:183], v[244:245]
	v_mov_b64_e32 v[184:185], v[246:247]
	v_pk_add_f32 v[162:163], v[162:163], 1.0 op_sel_hi:[1,0]
	v_pk_add_f32 v[160:161], v[160:161], 1.0 op_sel_hi:[1,0]
	v_pk_add_f32 v[158:159], v[158:159], 1.0 op_sel_hi:[1,0]
	v_pk_add_f32 v[156:157], v[156:157], 1.0 op_sel_hi:[1,0]
	s_waitcnt vmcnt(0)
	v_lshlrev_b32_e32 v5, 16, v182
	v_and_b32_e32 v181, 0xffff0000, v182
	v_lshlrev_b32_e32 v182, 16, v183
	v_and_b32_e32 v183, 0xffff0000, v183
	v_lshlrev_b32_e32 v186, 16, v184
	v_and_b32_e32 v184, 0xffff0000, v184
	v_lshlrev_b32_e32 v187, 16, v185
	v_and_b32_e32 v185, 0xffff0000, v185
	v_mul_f32_e32 v5, 0xbfb8aa3b, v5
	v_mul_f32_e32 v181, 0xbfb8aa3b, v181
	v_mul_f32_e32 v182, 0xbfb8aa3b, v182
	v_mul_f32_e32 v183, 0xbfb8aa3b, v183
	v_mul_f32_e32 v186, 0xbfb8aa3b, v186
	v_mul_f32_e32 v184, 0xbfb8aa3b, v184
	v_mul_f32_e32 v187, 0xbfb8aa3b, v187
	v_mul_f32_e32 v185, 0xbfb8aa3b, v185
	v_exp_f32_e32 v5, v5
	v_exp_f32_e32 v181, v181
	v_exp_f32_e32 v182, v182
	v_exp_f32_e32 v183, v183
	v_exp_f32_e32 v186, v186
	v_exp_f32_e32 v184, v184
	v_exp_f32_e32 v187, v187
	v_exp_f32_e32 v185, v185
	v_add_f32_e32 v5, 1.0, v5
	v_add_f32_e32 v181, 1.0, v181
	v_add_f32_e32 v188, 1.0, v182
	v_add_f32_e32 v189, 1.0, v183
	v_add_f32_e32 v186, 1.0, v186
	v_add_f32_e32 v190, 1.0, v184
	v_add_f32_e32 v191, 1.0, v187
	v_add_f32_e32 v192, 1.0, v185
	v_rcp_f32_e32 v182, v5
	v_rcp_f32_e32 v183, v181
	v_rcp_f32_e32 v184, v188
	v_rcp_f32_e32 v185, v189
	v_rcp_f32_e32 v186, v186
	v_rcp_f32_e32 v187, v190
	v_rcp_f32_e32 v188, v191
	v_rcp_f32_e32 v189, v192
	v_pk_mul_f32 v[160:161], v[160:161], v[182:183]
	v_pk_mul_f32 v[162:163], v[162:163], v[184:185]
	v_pk_mul_f32 v[156:157], v[156:157], v[186:187]
	v_pk_mul_f32 v[158:159], v[158:159], v[188:189]
	v_pk_mul_f32 v[64:65], v[64:65], v[162:163]
	v_pk_mul_f32 v[62:63], v[62:63], v[160:161]
	v_pk_mul_f32 v[60:61], v[60:61], v[158:159]
	v_pk_mul_f32 v[58:59], v[58:59], v[156:157]
.LBB0_605:
	v_mov_b64_e32 v[156:157], v[240:241]
	v_mov_b64_e32 v[158:159], v[242:243]
	s_and_b64 vcc, exec, s[4:5]
	s_mov_b64 s[58:59], -1
	s_waitcnt vmcnt(0)
	v_lshlrev_b32_e32 v5, 16, v156
	v_and_b32_e32 v8, 0xffff0000, v156
	v_lshlrev_b32_e32 v9, 16, v157
	v_and_b32_e32 v156, 0xffff0000, v157
	v_lshlrev_b32_e32 v157, 16, v158
	v_and_b32_e32 v158, 0xffff0000, v158
	v_lshlrev_b32_e32 v160, 16, v159
	v_and_b32_e32 v159, 0xffff0000, v159
	v_mul_f32_e32 v5, 0xbfb8aa3b, v5
	v_mul_f32_e32 v8, 0xbfb8aa3b, v8
	v_mul_f32_e32 v9, 0xbfb8aa3b, v9
	v_mul_f32_e32 v156, 0xbfb8aa3b, v156
	v_mul_f32_e32 v157, 0xbfb8aa3b, v157
	v_mul_f32_e32 v162, 0xbfb8aa3b, v158
	v_mul_f32_e32 v163, 0xbfb8aa3b, v160
	v_mul_f32_e32 v181, 0xbfb8aa3b, v159
	v_exp_f32_e32 v158, v5
	v_exp_f32_e32 v159, v8
	v_exp_f32_e32 v160, v9
	v_exp_f32_e32 v161, v156
	v_exp_f32_e32 v8, v157
	v_exp_f32_e32 v9, v162
	v_exp_f32_e32 v156, v163
	v_exp_f32_e32 v157, v181
	s_cbranch_vccnz .LBB0_634
	v_add_f32_e32 v162, 1.0, v159
	v_add_f32_e32 v163, 1.0, v160
	v_rcp_f32_e32 v162, v162
	v_rcp_f32_e32 v163, v163
	v_add_f32_e32 v182, 1.0, v8
	v_rcp_f32_e32 v182, v182
	v_mul_f32_e32 v162, v31, v162
	v_mul_f32_e32 v181, 0x3c000000, v162
	v_mul_f32_e32 v162, v32, v163
	v_add_f32_e32 v163, 1.0, v161
	v_rcp_f32_e32 v163, v163
	v_mul_f32_e32 v183, 0x3c000000, v162
	v_add_f32_e32 v5, 1.0, v158
	v_rcp_f32_e32 v5, v5
	v_mul_f32_e32 v162, v33, v163
	v_add_f32_e32 v163, 1.0, v9
	v_mul_f32_e32 v184, 0x3c000000, v162
	v_mul_f32_e32 v162, v26, v182
	v_rcp_f32_e32 v163, v163
	v_add_f32_e32 v182, 1.0, v156
	v_rcp_f32_e32 v182, v182
	v_mul_f32_e32 v185, 0x3c000000, v162
	v_mul_f32_e32 v162, v27, v163
	v_mul_f32_e32 v186, 0x3c000000, v162
	v_mul_f32_e32 v162, v28, v182
	v_mul_f32_e32 v182, 0x3c000000, v162
	v_add_f32_e32 v162, 1.0, v157
	v_mul_f32_e32 v5, v30, v5
	v_rcp_f32_e32 v187, v162
	v_mul_f32_e32 v5, 0x3c000000, v5
	v_mov_b32_e32 v162, 0
	v_mov_b32_e32 v163, 0
	v_cvt_pk_fp8_f32 v162, v5, v181
	v_cvt_pk_fp8_f32 v163, v185, v186
	v_mul_f32_e32 v5, v29, v187
	v_mul_f32_e32 v5, 0x3c000000, v5
	v_cvt_pk_fp8_f32 v162, v183, v184 op_sel:[0,0,1]
	v_cvt_pk_fp8_f32 v163, v182, v5 op_sel:[0,0,1]
	ds_write_b64 v180, v[162:163] offset:32
	s_cbranch_execz .LBB0_635

; #define LAS __attribute__((address_space(3)))
; __device__ __forceinline__ unsigned pk4_fp8(float a, float b, float c, float d) { int w = 0; w = __builtin_amdgcn_cvt_pk_fp8_f32(a, b, w, false); w = __builtin_amdgcn_cvt_pk_fp8_f32(c, d, w, true); return (unsigned)w; }
; __device__ __forceinline__ float bf_lo(unsigned w) { return __uint_as_float(w << 16); }
; __device__ __forceinline__ float bf_hi(unsigned w) { return __uint_as_float(w & 0xffff0000u); }
; __device__ __forceinline__ float sigmoidf_fast(float x) { return __builtin_amdgcn_rcpf(1.0f + __builtin_amdgcn_exp2f(-1.4426950408889634f * x)); }
;     __device__ __forceinline__ void operator()(f32x4 (&acc)[2][2][4][2], const Unit& u, int wr, int wc, int fr, int fq) const {
;     ...
;                 const size_t ro = (size_t)(u.row0 + ai * 128 + wr * 64 + m * 16 + fr) * DM + col0;
; #pragma unroll
;                 for (int bj = 0; bj < 2; ++bj) {
;                     const u32x4 gd = *(const u32x4*)(GDF + ro + bj * 32);
;                     const float ed[8] = {bf_lo(gd.x), bf_hi(gd.x), bf_lo(gd.y), bf_hi(gd.y), bf_lo(gd.z), bf_hi(gd.z), bf_lo(gd.w), bf_hi(gd.w)};
;                     if (u.tag == 0) {
;                         const u32x4 gn = *(const u32x4*)(GNA + ro + bj * 32);
;                         const float en[8] = {bf_lo(gn.x), bf_hi(gn.x), bf_lo(gn.y), bf_hi(gn.y), bf_lo(gn.z), bf_hi(gn.z), bf_lo(gn.w), bf_hi(gn.w)};
; #pragma unroll
;                         for (int e = 0; e < 8; ++e) {
;                             const float r = (1.0f + __builtin_amdgcn_exp2f(-1.4426950408889634f * ed[e])) * __builtin_amdgcn_rcpf(1.0f + __builtin_amdgcn_exp2f(-1.4426950408889634f * en[e]));
;                             acc[ai][bj][m][e >> 2][e & 3] *= r; }
;                     } else {
;                         float y[8];
; #pragma unroll
;                         for (int e = 0; e < 8; ++e) y[e] = acc[ai][bj][m][e >> 2][e & 3] * sigmoidf_fast(ed[e]) * (PSCALE * WSCALE_INV * OSCALE_INV);
;                         u32x2 w; w.x = pk4_fp8(y[0], y[1], y[2], y[3]); w.y = pk4_fp8(y[4], y[5], y[6], y[7]);
;                         *(LAS u32x2*)(my + fr * 80 + bj * 32 + fq * 8) = w;
;                     }
;                 }
.LBB0_609:
	s_nop 1
	v_add_u32_e32 v6, 0xa0, v4
	v_ashrrev_i32_e32 v7, 31, v6
	v_lshlrev_b64 v[6:7], 11, v[6:7]
	v_lshl_add_u64 v[6:7], v[6:7], 0, v[2:3]
	v_lshl_add_u64 v[8:9], v[6:7], 1, s[40:41]
	global_load_dwordx4 v[156:159], v[8:9], off nt
	global_load_dwordx4 v[240:243], v[8:9], off offset:64 nt
	v_lshl_add_u64 v[252:253], v[6:7], 1, s[38:39]
	global_load_dwordx4 v[244:247], v[252:253], off nt
	s_and_b64 vcc, exec, s[4:5]
	s_mov_b64 s[58:59], -1
	s_waitcnt vmcnt(0)
	v_lshlrev_b32_e32 v5, 16, v156
	v_and_b32_e32 v156, 0xffff0000, v156
	v_lshlrev_b32_e32 v160, 16, v157
	v_and_b32_e32 v157, 0xffff0000, v157
	v_lshlrev_b32_e32 v161, 16, v158
	v_and_b32_e32 v158, 0xffff0000, v158
	v_lshlrev_b32_e32 v162, 16, v159
	v_and_b32_e32 v159, 0xffff0000, v159
	v_mul_f32_e32 v5, 0xbfb8aa3b, v5
	v_mul_f32_e32 v156, 0xbfb8aa3b, v156
	v_mul_f32_e32 v163, 0xbfb8aa3b, v160
	v_mul_f32_e32 v157, 0xbfb8aa3b, v157
	v_mul_f32_e32 v181, 0xbfb8aa3b, v161
	v_mul_f32_e32 v158, 0xbfb8aa3b, v158
	v_mul_f32_e32 v182, 0xbfb8aa3b, v162
	v_mul_f32_e32 v159, 0xbfb8aa3b, v159
	v_exp_f32_e32 v160, v5
	v_exp_f32_e32 v161, v156
	v_exp_f32_e32 v162, v163
	v_exp_f32_e32 v163, v157
	v_exp_f32_e32 v156, v181
	v_exp_f32_e32 v157, v158
	v_exp_f32_e32 v158, v182
	v_exp_f32_e32 v159, v159
	s_cbranch_vccnz .LBB0_611
	v_add_f32_e32 v182, 1.0, v162
	v_rcp_f32_e32 v182, v182
	v_add_f32_e32 v183, 1.0, v163
	v_rcp_f32_e32 v183, v183
	v_add_f32_e32 v184, 1.0, v156
	v_rcp_f32_e32 v184, v184
	v_mul_f32_e32 v182, v56, v182
	v_mul_f32_e32 v185, 0x3c000000, v182
	v_mul_f32_e32 v182, v57, v183
	v_add_f32_e32 v183, 1.0, v157
	v_mul_f32_e32 v186, 0x3c000000, v182
	v_mul_f32_e32 v182, v50, v184
	v_rcp_f32_e32 v183, v183
	v_add_f32_e32 v184, 1.0, v158
	v_rcp_f32_e32 v184, v184
	v_add_f32_e32 v5, 1.0, v160
	v_add_f32_e32 v181, 1.0, v161
	v_rcp_f32_e32 v5, v5
	v_rcp_f32_e32 v181, v181
	v_mul_f32_e32 v187, 0x3c000000, v182
	v_mul_f32_e32 v182, v51, v183
	v_mul_f32_e32 v188, 0x3c000000, v182
	v_mul_f32_e32 v182, v52, v184
	v_mul_f32_e32 v184, 0x3c000000, v182
	v_add_f32_e32 v182, 1.0, v159
	v_mul_f32_e32 v5, v54, v5
	v_mul_f32_e32 v181, v55, v181
	v_rcp_f32_e32 v189, v182
	v_mul_f32_e32 v5, 0x3c000000, v5
	v_mul_f32_e32 v181, 0x3c000000, v181
	v_mov_b32_e32 v182, 0
	v_mov_b32_e32 v183, 0
	v_cvt_pk_fp8_f32 v182, v5, v181
	v_cvt_pk_fp8_f32 v183, v187, v188
	v_mul_f32_e32 v5, v53, v189
	v_mul_f32_e32 v5, 0x3c000000, v5
	v_cvt_pk_fp8_f32 v182, v185, v186 op_sel:[0,0,1]
	v_cvt_pk_fp8_f32 v183, v184, v5 op_sel:[0,0,1]
	s_mov_b64 s[58:59], 0
	ds_write_b64 v180, v[182:183]
.LBB0_611:
	s_andn2_b64 vcc, exec, s[58:59]
	v_lshl_add_u64 v[6:7], v[6:7], 1, s[38:39]
	s_cbranch_vccnz .LBB0_613
	v_mov_b64_e32 v[182:183], v[244:245]
	v_mov_b64_e32 v[184:185], v[246:247]
	v_pk_add_f32 v[162:163], v[162:163], 1.0 op_sel_hi:[1,0]
	v_pk_add_f32 v[160:161], v[160:161], 1.0 op_sel_hi:[1,0]
	v_pk_add_f32 v[158:159], v[158:159], 1.0 op_sel_hi:[1,0]
	v_pk_add_f32 v[156:157], v[156:157], 1.0 op_sel_hi:[1,0]
	s_waitcnt vmcnt(0)
	v_lshlrev_b32_e32 v5, 16, v182
	v_and_b32_e32 v181, 0xffff0000, v182
	v_lshlrev_b32_e32 v182, 16, v183
	v_and_b32_e32 v183, 0xffff0000, v183
	v_lshlrev_b32_e32 v186, 16, v184
	v_and_b32_e32 v184, 0xffff0000, v184
	v_lshlrev_b32_e32 v187, 16, v185
	v_and_b32_e32 v185, 0xffff0000, v185
	v_mul_f32_e32 v5, 0xbfb8aa3b, v5
	v_mul_f32_e32 v181, 0xbfb8aa3b, v181
	v_mul_f32_e32 v182, 0xbfb8aa3b, v182
	v_mul_f32_e32 v183, 0xbfb8aa3b, v183
	v_mul_f32_e32 v186, 0xbfb8aa3b, v186
	v_mul_f32_e32 v184, 0xbfb8aa3b, v184
	v_mul_f32_e32 v187, 0xbfb8aa3b, v187
	v_mul_f32_e32 v185, 0xbfb8aa3b, v185
	v_exp_f32_e32 v5, v5
	v_exp_f32_e32 v181, v181
	v_exp_f32_e32 v182, v182
	v_exp_f32_e32 v183, v183
	v_exp_f32_e32 v186, v186
	v_exp_f32_e32 v184, v184
	v_exp_f32_e32 v187, v187
	v_exp_f32_e32 v185, v185
	v_add_f32_e32 v5, 1.0, v5
	v_add_f32_e32 v181, 1.0, v181
	v_add_f32_e32 v188, 1.0, v182
	v_add_f32_e32 v189, 1.0, v183
	v_add_f32_e32 v186, 1.0, v186
	v_add_f32_e32 v190, 1.0, v184
	v_add_f32_e32 v191, 1.0, v187
	v_add_f32_e32 v192, 1.0, v185
	v_rcp_f32_e32 v182, v5
	v_rcp_f32_e32 v183, v181
	v_rcp_f32_e32 v184, v188
	v_rcp_f32_e32 v185, v189
	v_rcp_f32_e32 v186, v186
	v_rcp_f32_e32 v187, v190
	v_rcp_f32_e32 v188, v191
	v_rcp_f32_e32 v189, v192
	v_pk_mul_f32 v[160:161], v[160:161], v[182:183]
	v_pk_mul_f32 v[162:163], v[162:163], v[184:185]
	v_pk_mul_f32 v[156:157], v[156:157], v[186:187]
	v_pk_mul_f32 v[158:159], v[158:159], v[188:189]
	v_pk_mul_f32 v[56:57], v[56:57], v[162:163]
	v_pk_mul_f32 v[54:55], v[54:55], v[160:161]
	v_pk_mul_f32 v[52:53], v[52:53], v[158:159]
	v_pk_mul_f32 v[50:51], v[50:51], v[156:157]
.LBB0_613:
	v_mov_b64_e32 v[156:157], v[240:241]
	v_mov_b64_e32 v[158:159], v[242:243]
	s_and_b64 vcc, exec, s[4:5]
	s_mov_b64 s[58:59], -1
	s_waitcnt vmcnt(0)
	v_lshlrev_b32_e32 v5, 16, v156
	v_and_b32_e32 v8, 0xffff0000, v156
	v_lshlrev_b32_e32 v9, 16, v157
	v_and_b32_e32 v156, 0xffff0000, v157
	v_lshlrev_b32_e32 v157, 16, v158
	v_and_b32_e32 v158, 0xffff0000, v158
	v_lshlrev_b32_e32 v160, 16, v159
	v_and_b32_e32 v159, 0xffff0000, v159
	v_mul_f32_e32 v5, 0xbfb8aa3b, v5
	v_mul_f32_e32 v8, 0xbfb8aa3b, v8
	v_mul_f32_e32 v9, 0xbfb8aa3b, v9
	v_mul_f32_e32 v156, 0xbfb8aa3b, v156
	v_mul_f32_e32 v157, 0xbfb8aa3b, v157
	v_mul_f32_e32 v162, 0xbfb8aa3b, v158
	v_mul_f32_e32 v163, 0xbfb8aa3b, v160
	v_mul_f32_e32 v181, 0xbfb8aa3b, v159
	v_exp_f32_e32 v158, v5
	v_exp_f32_e32 v159, v8
	v_exp_f32_e32 v160, v9
	v_exp_f32_e32 v161, v156
	v_exp_f32_e32 v8, v157
	v_exp_f32_e32 v9, v162
	v_exp_f32_e32 v156, v163
	v_exp_f32_e32 v157, v181
	s_cbranch_vccnz .LBB0_636
	v_add_f32_e32 v162, 1.0, v159
	v_add_f32_e32 v163, 1.0, v160
	v_rcp_f32_e32 v162, v162
	v_rcp_f32_e32 v163, v163
	v_add_f32_e32 v182, 1.0, v8
	v_rcp_f32_e32 v182, v182
	v_mul_f32_e32 v162, v23, v162
	v_mul_f32_e32 v181, 0x3c000000, v162
	v_mul_f32_e32 v162, v24, v163
	v_add_f32_e32 v163, 1.0, v161
	v_rcp_f32_e32 v163, v163
	v_mul_f32_e32 v183, 0x3c000000, v162
	v_add_f32_e32 v5, 1.0, v158
	v_rcp_f32_e32 v5, v5
	v_mul_f32_e32 v162, v25, v163
	v_add_f32_e32 v163, 1.0, v9
	v_mul_f32_e32 v184, 0x3c000000, v162
	v_mul_f32_e32 v162, v18, v182
	v_rcp_f32_e32 v163, v163
	v_add_f32_e32 v182, 1.0, v156
	v_rcp_f32_e32 v182, v182
	v_mul_f32_e32 v185, 0x3c000000, v162
	v_mul_f32_e32 v162, v19, v163
	v_mul_f32_e32 v186, 0x3c000000, v162
	v_mul_f32_e32 v162, v20, v182
	v_mul_f32_e32 v182, 0x3c000000, v162
	v_add_f32_e32 v162, 1.0, v157
	v_mul_f32_e32 v5, v22, v5
	v_rcp_f32_e32 v187, v162
	v_mul_f32_e32 v5, 0x3c000000, v5
	v_mov_b32_e32 v162, 0
	v_mov_b32_e32 v163, 0
	v_cvt_pk_fp8_f32 v162, v5, v181
	v_cvt_pk_fp8_f32 v163, v185, v186
	v_mul_f32_e32 v5, v21, v187
	v_mul_f32_e32 v5, 0x3c000000, v5
	v_cvt_pk_fp8_f32 v162, v183, v184 op_sel:[0,0,1]
	v_cvt_pk_fp8_f32 v163, v182, v5 op_sel:[0,0,1]
	ds_write_b64 v180, v[162:163] offset:32
	s_cbranch_execz .LBB0_637

; #define LAS __attribute__((address_space(3)))
; __device__ __forceinline__ unsigned pk4_fp8(float a, float b, float c, float d) { int w = 0; w = __builtin_amdgcn_cvt_pk_fp8_f32(a, b, w, false); w = __builtin_amdgcn_cvt_pk_fp8_f32(c, d, w, true); return (unsigned)w; }
; __device__ __forceinline__ float bf_lo(unsigned w) { return __uint_as_float(w << 16); }
; __device__ __forceinline__ float bf_hi(unsigned w) { return __uint_as_float(w & 0xffff0000u); }
; __device__ __forceinline__ float sigmoidf_fast(float x) { return __builtin_amdgcn_rcpf(1.0f + __builtin_amdgcn_exp2f(-1.4426950408889634f * x)); }
;     __device__ __forceinline__ void operator()(f32x4 (&acc)[2][2][4][2], const Unit& u, int wr, int wc, int fr, int fq) const {
;     ...
;                 const size_t ro = (size_t)(u.row0 + ai * 128 + wr * 64 + m * 16 + fr) * DM + col0;
; #pragma unroll
;                 for (int bj = 0; bj < 2; ++bj) {
;                     const u32x4 gd = *(const u32x4*)(GDF + ro + bj * 32);
;                     const float ed[8] = {bf_lo(gd.x), bf_hi(gd.x), bf_lo(gd.y), bf_hi(gd.y), bf_lo(gd.z), bf_hi(gd.z), bf_lo(gd.w), bf_hi(gd.w)};
;                     if (u.tag == 0) {
;                         const u32x4 gn = *(const u32x4*)(GNA + ro + bj * 32);
;                         const float en[8] = {bf_lo(gn.x), bf_hi(gn.x), bf_lo(gn.y), bf_hi(gn.y), bf_lo(gn.z), bf_hi(gn.z), bf_lo(gn.w), bf_hi(gn.w)};
; #pragma unroll
;                         for (int e = 0; e < 8; ++e) {
;                             const float r = (1.0f + __builtin_amdgcn_exp2f(-1.4426950408889634f * ed[e])) * __builtin_amdgcn_rcpf(1.0f + __builtin_amdgcn_exp2f(-1.4426950408889634f * en[e]));
;                             acc[ai][bj][m][e >> 2][e & 3] *= r; }
;                     } else {
;                         float y[8];
; #pragma unroll
;                         for (int e = 0; e < 8; ++e) y[e] = acc[ai][bj][m][e >> 2][e & 3] * sigmoidf_fast(ed[e]) * (PSCALE * WSCALE_INV * OSCALE_INV);
;                         u32x2 w; w.x = pk4_fp8(y[0], y[1], y[2], y[3]); w.y = pk4_fp8(y[4], y[5], y[6], y[7]);
;                         *(LAS u32x2*)(my + fr * 80 + bj * 32 + fq * 8) = w;
;                     }
;                 }
.LBB0_617:
	v_add_u32_e32 v4, 0xb0, v4
	v_ashrrev_i32_e32 v5, 31, v4
	v_lshlrev_b64 v[4:5], 11, v[4:5]
	v_lshl_add_u64 v[2:3], v[4:5], 0, v[2:3]
	v_lshl_add_u64 v[4:5], v[2:3], 1, s[40:41]
	global_load_dwordx4 v[6:9], v[4:5], off nt
	global_load_dwordx4 v[240:243], v[4:5], off offset:64 nt
	v_lshl_add_u64 v[252:253], v[2:3], 1, s[38:39]
	global_load_dwordx4 v[244:247], v[252:253], off nt
	s_and_b64 vcc, exec, s[4:5]
	s_mov_b64 s[58:59], -1
	s_waitcnt vmcnt(0)
	v_lshlrev_b32_e32 v156, 16, v6
	v_and_b32_e32 v6, 0xffff0000, v6
	v_lshlrev_b32_e32 v157, 16, v7
	v_and_b32_e32 v7, 0xffff0000, v7
	v_lshlrev_b32_e32 v158, 16, v8
	v_and_b32_e32 v8, 0xffff0000, v8
	v_lshlrev_b32_e32 v159, 16, v9
	v_and_b32_e32 v9, 0xffff0000, v9
	v_mul_f32_e32 v156, 0xbfb8aa3b, v156
	v_mul_f32_e32 v6, 0xbfb8aa3b, v6
	v_mul_f32_e32 v160, 0xbfb8aa3b, v157
	v_mul_f32_e32 v7, 0xbfb8aa3b, v7
	v_mul_f32_e32 v161, 0xbfb8aa3b, v158
	v_mul_f32_e32 v8, 0xbfb8aa3b, v8
	v_mul_f32_e32 v162, 0xbfb8aa3b, v159
	v_mul_f32_e32 v9, 0xbfb8aa3b, v9
	v_exp_f32_e32 v156, v156
	v_exp_f32_e32 v157, v6
	v_exp_f32_e32 v158, v160
	v_exp_f32_e32 v159, v7
	v_exp_f32_e32 v6, v161
	v_exp_f32_e32 v7, v8
	v_exp_f32_e32 v8, v162
	v_exp_f32_e32 v9, v9
	s_cbranch_vccnz .LBB0_619
	v_add_f32_e32 v160, 1.0, v156
	v_rcp_f32_e32 v160, v160
	v_add_f32_e32 v161, 1.0, v157
	v_add_f32_e32 v162, 1.0, v158
	v_rcp_f32_e32 v161, v161
	v_rcp_f32_e32 v162, v162
	v_mul_f32_e32 v160, v46, v160
	v_mul_f32_e32 v163, 0x3c000000, v160
	v_mul_f32_e32 v160, v47, v161
	v_mul_f32_e32 v161, 0x3c000000, v160
	v_mul_f32_e32 v160, v48, v162
	v_add_f32_e32 v162, 1.0, v159
	v_rcp_f32_e32 v162, v162
	v_add_f32_e32 v181, 1.0, v6
	v_rcp_f32_e32 v181, v181
	v_mul_f32_e32 v182, 0x3c000000, v160
	v_mul_f32_e32 v160, v49, v162
	v_mul_f32_e32 v162, 0x3c000000, v160
	v_mul_f32_e32 v160, v42, v181
	v_add_f32_e32 v181, 1.0, v7
	v_rcp_f32_e32 v181, v181
	v_add_f32_e32 v183, 1.0, v8
	v_rcp_f32_e32 v183, v183
	v_mul_f32_e32 v184, 0x3c000000, v160
	v_mul_f32_e32 v160, v43, v181
	v_mul_f32_e32 v181, 0x3c000000, v160
	v_mul_f32_e32 v160, v44, v183
	v_mul_f32_e32 v183, 0x3c000000, v160
	v_add_f32_e32 v160, 1.0, v9
	v_rcp_f32_e32 v185, v160
	v_mov_b32_e32 v160, 0
	v_cvt_pk_fp8_f32 v160, v163, v161
	v_mov_b32_e32 v161, 0
	v_cvt_pk_fp8_f32 v161, v184, v181
	v_mul_f32_e32 v163, v45, v185
	v_mul_f32_e32 v163, 0x3c000000, v163
	v_cvt_pk_fp8_f32 v160, v182, v162 op_sel:[0,0,1]
	v_cvt_pk_fp8_f32 v161, v183, v163 op_sel:[0,0,1]
	s_mov_b64 s[58:59], 0
	ds_write_b64 v180, v[160:161]
.LBB0_619:
	s_andn2_b64 vcc, exec, s[58:59]
	v_lshl_add_u64 v[2:3], v[2:3], 1, s[38:39]
	s_cbranch_vccnz .LBB0_621
	v_mov_b64_e32 v[160:161], v[244:245]
	v_mov_b64_e32 v[162:163], v[246:247]
	v_pk_add_f32 v[158:159], v[158:159], 1.0 op_sel_hi:[1,0]
	v_pk_add_f32 v[156:157], v[156:157], 1.0 op_sel_hi:[1,0]
	v_pk_add_f32 v[8:9], v[8:9], 1.0 op_sel_hi:[1,0]
	v_pk_add_f32 v[6:7], v[6:7], 1.0 op_sel_hi:[1,0]
	s_waitcnt vmcnt(0)
	v_lshlrev_b32_e32 v181, 16, v160
	v_and_b32_e32 v160, 0xffff0000, v160
	v_lshlrev_b32_e32 v182, 16, v161
	v_and_b32_e32 v161, 0xffff0000, v161
	v_lshlrev_b32_e32 v183, 16, v162
	v_and_b32_e32 v162, 0xffff0000, v162
	v_lshlrev_b32_e32 v184, 16, v163
	v_and_b32_e32 v163, 0xffff0000, v163
	v_mul_f32_e32 v181, 0xbfb8aa3b, v181
	v_mul_f32_e32 v160, 0xbfb8aa3b, v160
	v_mul_f32_e32 v182, 0xbfb8aa3b, v182
	v_mul_f32_e32 v161, 0xbfb8aa3b, v161
	v_mul_f32_e32 v183, 0xbfb8aa3b, v183
	v_mul_f32_e32 v162, 0xbfb8aa3b, v162
	v_mul_f32_e32 v184, 0xbfb8aa3b, v184
	v_mul_f32_e32 v163, 0xbfb8aa3b, v163
	v_exp_f32_e32 v181, v181
	v_exp_f32_e32 v160, v160
	v_exp_f32_e32 v182, v182
	v_exp_f32_e32 v161, v161
	v_exp_f32_e32 v183, v183
	v_exp_f32_e32 v162, v162
	v_exp_f32_e32 v184, v184
	v_exp_f32_e32 v163, v163
	v_add_f32_e32 v181, 1.0, v181
	v_add_f32_e32 v185, 1.0, v160
	v_add_f32_e32 v182, 1.0, v182
	v_add_f32_e32 v186, 1.0, v161
	v_add_f32_e32 v183, 1.0, v183
	v_add_f32_e32 v187, 1.0, v162
	v_add_f32_e32 v184, 1.0, v184
	v_add_f32_e32 v188, 1.0, v163
	v_rcp_f32_e32 v160, v181
	v_rcp_f32_e32 v161, v185
	v_rcp_f32_e32 v162, v182
	v_rcp_f32_e32 v163, v186
	v_rcp_f32_e32 v182, v183
	v_rcp_f32_e32 v183, v187
	v_rcp_f32_e32 v184, v184
	v_rcp_f32_e32 v185, v188
	v_pk_mul_f32 v[156:157], v[156:157], v[160:161]
	v_pk_mul_f32 v[158:159], v[158:159], v[162:163]
	v_pk_mul_f32 v[6:7], v[6:7], v[182:183]
	v_pk_mul_f32 v[8:9], v[8:9], v[184:185]
	v_pk_mul_f32 v[48:49], v[48:49], v[158:159]
	v_pk_mul_f32 v[46:47], v[46:47], v[156:157]
	v_pk_mul_f32 v[44:45], v[44:45], v[8:9]
	v_pk_mul_f32 v[42:43], v[42:43], v[6:7]
.LBB0_621:
	v_mov_b64_e32 v[4:5], v[240:241]
	v_mov_b64_e32 v[6:7], v[242:243]
	s_and_b64 vcc, exec, s[4:5]
	s_mov_b64 s[4:5], -1
	s_waitcnt vmcnt(0)
	v_lshlrev_b32_e32 v8, 16, v4
	v_and_b32_e32 v4, 0xffff0000, v4
	v_lshlrev_b32_e32 v9, 16, v5
	v_and_b32_e32 v5, 0xffff0000, v5
	v_lshlrev_b32_e32 v156, 16, v6
	v_and_b32_e32 v6, 0xffff0000, v6
	v_lshlrev_b32_e32 v157, 16, v7
	v_and_b32_e32 v7, 0xffff0000, v7
	v_mul_f32_e32 v8, 0xbfb8aa3b, v8
	v_mul_f32_e32 v4, 0xbfb8aa3b, v4
	v_mul_f32_e32 v158, 0xbfb8aa3b, v9
	v_mul_f32_e32 v5, 0xbfb8aa3b, v5
	v_mul_f32_e32 v159, 0xbfb8aa3b, v156
	v_mul_f32_e32 v6, 0xbfb8aa3b, v6
	v_mul_f32_e32 v160, 0xbfb8aa3b, v157
	v_mul_f32_e32 v7, 0xbfb8aa3b, v7
	v_exp_f32_e32 v8, v8
	v_exp_f32_e32 v9, v4
	v_exp_f32_e32 v156, v158
	v_exp_f32_e32 v157, v5
	v_exp_f32_e32 v4, v159
	v_exp_f32_e32 v5, v6
	v_exp_f32_e32 v6, v160
	v_exp_f32_e32 v7, v7
	s_cbranch_vccnz .LBB0_638
	v_add_f32_e32 v158, 1.0, v8
	v_rcp_f32_e32 v158, v158
	v_add_f32_e32 v159, 1.0, v9
	v_add_f32_e32 v160, 1.0, v156
	v_rcp_f32_e32 v159, v159
	v_rcp_f32_e32 v160, v160
	v_mul_f32_e32 v158, v14, v158
	v_mul_f32_e32 v161, 0x3c000000, v158
	v_mul_f32_e32 v158, v15, v159
	v_mul_f32_e32 v159, 0x3c000000, v158
	v_mul_f32_e32 v158, v16, v160
	v_add_f32_e32 v160, 1.0, v157
	v_rcp_f32_e32 v160, v160
	v_add_f32_e32 v162, 1.0, v4
	v_rcp_f32_e32 v162, v162
	v_mul_f32_e32 v163, 0x3c000000, v158
	v_mul_f32_e32 v158, v17, v160
	v_mul_f32_e32 v160, 0x3c000000, v158
	v_mul_f32_e32 v158, v10, v162
	v_add_f32_e32 v162, 1.0, v5
	v_rcp_f32_e32 v162, v162
	v_add_f32_e32 v181, 1.0, v6
	v_rcp_f32_e32 v181, v181
	v_mul_f32_e32 v182, 0x3c000000, v158
	v_mul_f32_e32 v158, v11, v162
	v_mul_f32_e32 v162, 0x3c000000, v158
	v_mul_f32_e32 v158, v12, v181
	v_mul_f32_e32 v181, 0x3c000000, v158
	v_add_f32_e32 v158, 1.0, v7
	v_rcp_f32_e32 v183, v158
	v_mov_b32_e32 v158, 0
	v_cvt_pk_fp8_f32 v158, v161, v159
	v_mov_b32_e32 v159, 0
	v_cvt_pk_fp8_f32 v159, v182, v162
	v_mul_f32_e32 v161, v13, v183
	v_mul_f32_e32 v161, 0x3c000000, v161
	v_cvt_pk_fp8_f32 v158, v163, v160 op_sel:[0,0,1]
	v_cvt_pk_fp8_f32 v159, v181, v161 op_sel:[0,0,1]
	ds_write_b64 v180, v[158:159] offset:32
	s_cbranch_execz .LBB0_639
